# residual epilogues hand-scheduled + start stagger; expert-table lookup deferred into K-loop; accumulator zeroing once per unit with 64-bit moves (skip-path zeroing out of line)
# speedup vs baseline: 1.0103x; 1.0050x over previous
.Lzs_0:
	v_mov_b64_e32 v[2:3], 0
	v_mov_b64_e32 v[4:5], 0
	v_mov_b64_e32 v[6:7], 0
	v_mov_b64_e32 v[8:9], 0
	v_mov_b64_e32 v[10:11], 0
	v_mov_b64_e32 v[12:13], 0
	v_mov_b64_e32 v[14:15], 0
	v_mov_b64_e32 v[16:17], 0
	v_mov_b64_e32 v[18:19], 0
	v_mov_b64_e32 v[20:21], 0
	v_mov_b64_e32 v[22:23], 0
	v_mov_b64_e32 v[24:25], 0
	v_mov_b64_e32 v[26:27], 0
	v_mov_b64_e32 v[28:29], 0
	v_mov_b64_e32 v[30:31], 0
	v_mov_b64_e32 v[32:33], 0
	v_mov_b64_e32 v[34:35], 0
	v_mov_b64_e32 v[36:37], 0
	v_mov_b64_e32 v[38:39], 0
	v_mov_b64_e32 v[40:41], 0
	v_mov_b64_e32 v[42:43], 0
	v_mov_b64_e32 v[44:45], 0
	v_mov_b64_e32 v[46:47], 0
	v_mov_b64_e32 v[48:49], 0
	v_mov_b64_e32 v[50:51], 0
	v_mov_b64_e32 v[52:53], 0
	v_mov_b64_e32 v[54:55], 0
	v_mov_b64_e32 v[56:57], 0
	v_mov_b64_e32 v[58:59], 0
	v_mov_b64_e32 v[60:61], 0
	v_mov_b64_e32 v[62:63], 0
	v_mov_b64_e32 v[64:65], 0
	v_mov_b64_e32 v[66:67], 0
	v_mov_b64_e32 v[68:69], 0
	v_mov_b64_e32 v[70:71], 0
	v_mov_b64_e32 v[72:73], 0
	v_mov_b64_e32 v[74:75], 0
	v_mov_b64_e32 v[76:77], 0
	v_mov_b64_e32 v[78:79], 0
	v_mov_b64_e32 v[80:81], 0
	v_mov_b64_e32 v[82:83], 0
	v_mov_b64_e32 v[84:85], 0
	v_mov_b64_e32 v[86:87], 0
	v_mov_b64_e32 v[88:89], 0
	v_mov_b64_e32 v[90:91], 0
	v_mov_b64_e32 v[92:93], 0
	v_mov_b64_e32 v[94:95], 0
	v_mov_b64_e32 v[96:97], 0
	v_mov_b64_e32 v[98:99], 0
	v_mov_b64_e32 v[100:101], 0
	v_mov_b64_e32 v[102:103], 0
	v_mov_b64_e32 v[104:105], 0
	v_mov_b64_e32 v[106:107], 0
	v_mov_b64_e32 v[108:109], 0
	v_mov_b64_e32 v[110:111], 0
	v_mov_b64_e32 v[112:113], 0
	v_mov_b64_e32 v[114:115], 0
	v_mov_b64_e32 v[116:117], 0
	v_mov_b64_e32 v[118:119], 0
	v_mov_b64_e32 v[120:121], 0
	v_mov_b64_e32 v[122:123], 0
	v_mov_b64_e32 v[124:125], 0
	v_mov_b64_e32 v[126:127], 0
	v_mov_b64_e32 v[128:129], 0
	s_branch .LBB0_297

.LBB0_294:
	s_andn2_b64 vcc, exec, s[8:9]
	s_waitcnt lgkmcnt(0)
	s_cbranch_vccnz .Lzs_0
	s_add_i32 s14, s71, 0x80
	s_addk_i32 s70, 0x100
	s_mov_b32 s71, 0
	v_mov_b64_e32 v[2:3], 0
	v_mov_b64_e32 v[4:5], 0
	v_mov_b64_e32 v[6:7], 0
	v_mov_b64_e32 v[8:9], 0
	v_mov_b64_e32 v[10:11], 0
	v_mov_b64_e32 v[12:13], 0
	v_mov_b64_e32 v[14:15], 0
	v_mov_b64_e32 v[16:17], 0
	v_mov_b64_e32 v[18:19], 0
	v_mov_b64_e32 v[20:21], 0
	v_mov_b64_e32 v[22:23], 0
	v_mov_b64_e32 v[24:25], 0
	v_mov_b64_e32 v[26:27], 0
	v_mov_b64_e32 v[28:29], 0
	v_mov_b64_e32 v[30:31], 0
	v_mov_b64_e32 v[32:33], 0
	v_mov_b64_e32 v[34:35], 0
	v_mov_b64_e32 v[36:37], 0
	v_mov_b64_e32 v[38:39], 0
	v_mov_b64_e32 v[40:41], 0
	v_mov_b64_e32 v[42:43], 0
	v_mov_b64_e32 v[44:45], 0
	v_mov_b64_e32 v[46:47], 0
	v_mov_b64_e32 v[48:49], 0
	v_mov_b64_e32 v[50:51], 0
	v_mov_b64_e32 v[52:53], 0
	v_mov_b64_e32 v[54:55], 0
	v_mov_b64_e32 v[56:57], 0
	v_mov_b64_e32 v[58:59], 0
	v_mov_b64_e32 v[60:61], 0
	v_mov_b64_e32 v[62:63], 0
	v_mov_b64_e32 v[64:65], 0
	v_mov_b64_e32 v[66:67], 0
	v_mov_b64_e32 v[68:69], 0
	v_mov_b64_e32 v[70:71], 0
	v_mov_b64_e32 v[72:73], 0
	v_mov_b64_e32 v[74:75], 0
	v_mov_b64_e32 v[76:77], 0
	v_mov_b64_e32 v[78:79], 0
	v_mov_b64_e32 v[80:81], 0
	v_mov_b64_e32 v[82:83], 0
	v_mov_b64_e32 v[84:85], 0
	v_mov_b64_e32 v[86:87], 0
	v_mov_b64_e32 v[88:89], 0
	v_mov_b64_e32 v[90:91], 0
	v_mov_b64_e32 v[92:93], 0
	v_mov_b64_e32 v[94:95], 0
	v_mov_b64_e32 v[96:97], 0
	v_mov_b64_e32 v[98:99], 0
	v_mov_b64_e32 v[100:101], 0
	v_mov_b64_e32 v[102:103], 0
	v_mov_b64_e32 v[104:105], 0
	v_mov_b64_e32 v[106:107], 0
	v_mov_b64_e32 v[108:109], 0
	v_mov_b64_e32 v[110:111], 0
	v_mov_b64_e32 v[112:113], 0
	v_mov_b64_e32 v[114:115], 0
	v_mov_b64_e32 v[116:117], 0
	v_mov_b64_e32 v[118:119], 0
	v_mov_b64_e32 v[120:121], 0
	v_mov_b64_e32 v[122:123], 0
	v_mov_b64_e32 v[124:125], 0
	v_mov_b64_e32 v[126:127], 0
	v_mov_b64_e32 v[128:129], 0

.LBB0_601:
	s_andn2_b64 vcc, exec, s[10:11]
	s_cbranch_vccnz .Lzs_1
	s_add_i32 s16, s74, 0x80
	s_addk_i32 s73, 0x100
	s_mov_b32 s74, 0
	v_mov_b64_e32 v[2:3], 0
	v_mov_b64_e32 v[4:5], 0
	v_mov_b64_e32 v[6:7], 0
	v_mov_b64_e32 v[8:9], 0
	v_mov_b64_e32 v[10:11], 0
	v_mov_b64_e32 v[12:13], 0
	v_mov_b64_e32 v[14:15], 0
	v_mov_b64_e32 v[16:17], 0
	v_mov_b64_e32 v[18:19], 0
	v_mov_b64_e32 v[20:21], 0
	v_mov_b64_e32 v[22:23], 0
	v_mov_b64_e32 v[24:25], 0
	v_mov_b64_e32 v[26:27], 0
	v_mov_b64_e32 v[28:29], 0
	v_mov_b64_e32 v[30:31], 0
	v_mov_b64_e32 v[32:33], 0
	v_mov_b64_e32 v[34:35], 0
	v_mov_b64_e32 v[36:37], 0
	v_mov_b64_e32 v[38:39], 0
	v_mov_b64_e32 v[40:41], 0
	v_mov_b64_e32 v[42:43], 0
	v_mov_b64_e32 v[44:45], 0
	v_mov_b64_e32 v[46:47], 0
	v_mov_b64_e32 v[48:49], 0
	v_mov_b64_e32 v[50:51], 0
	v_mov_b64_e32 v[52:53], 0
	v_mov_b64_e32 v[54:55], 0
	v_mov_b64_e32 v[56:57], 0
	v_mov_b64_e32 v[58:59], 0
	v_mov_b64_e32 v[60:61], 0
	v_mov_b64_e32 v[62:63], 0
	v_mov_b64_e32 v[64:65], 0
	v_mov_b64_e32 v[66:67], 0
	v_mov_b64_e32 v[68:69], 0
	v_mov_b64_e32 v[70:71], 0
	v_mov_b64_e32 v[72:73], 0
	v_mov_b64_e32 v[74:75], 0
	v_mov_b64_e32 v[76:77], 0
	v_mov_b64_e32 v[78:79], 0
	v_mov_b64_e32 v[80:81], 0
	v_mov_b64_e32 v[82:83], 0
	v_mov_b64_e32 v[84:85], 0
	v_mov_b64_e32 v[86:87], 0
	v_mov_b64_e32 v[88:89], 0
	v_mov_b64_e32 v[90:91], 0
	v_mov_b64_e32 v[92:93], 0
	v_mov_b64_e32 v[94:95], 0
	v_mov_b64_e32 v[96:97], 0
	v_mov_b64_e32 v[98:99], 0
	v_mov_b64_e32 v[100:101], 0
	v_mov_b64_e32 v[102:103], 0
	v_mov_b64_e32 v[104:105], 0
	v_mov_b64_e32 v[106:107], 0
	v_mov_b64_e32 v[108:109], 0
	v_mov_b64_e32 v[110:111], 0
	v_mov_b64_e32 v[112:113], 0
	v_mov_b64_e32 v[114:115], 0
	v_mov_b64_e32 v[116:117], 0
	v_mov_b64_e32 v[118:119], 0
	v_mov_b64_e32 v[120:121], 0
	v_mov_b64_e32 v[122:123], 0
	v_mov_b64_e32 v[124:125], 0
	v_mov_b64_e32 v[126:127], 0
	v_mov_b64_e32 v[128:129], 0

.LBB0_618:
	s_andn2_b64 vcc, exec, s[10:11]
	s_cbranch_vccnz .Lzs_2
	s_add_i32 s16, s72, 0x80
	s_addk_i32 s71, 0x100
	s_mov_b32 s72, 0
	v_mov_b64_e32 v[2:3], 0
	v_mov_b64_e32 v[4:5], 0
	v_mov_b64_e32 v[6:7], 0
	v_mov_b64_e32 v[8:9], 0
	v_mov_b64_e32 v[10:11], 0
	v_mov_b64_e32 v[12:13], 0
	v_mov_b64_e32 v[14:15], 0
	v_mov_b64_e32 v[16:17], 0
	v_mov_b64_e32 v[18:19], 0
	v_mov_b64_e32 v[20:21], 0
	v_mov_b64_e32 v[22:23], 0
	v_mov_b64_e32 v[24:25], 0
	v_mov_b64_e32 v[26:27], 0
	v_mov_b64_e32 v[28:29], 0
	v_mov_b64_e32 v[30:31], 0
	v_mov_b64_e32 v[32:33], 0
	v_mov_b64_e32 v[34:35], 0
	v_mov_b64_e32 v[36:37], 0
	v_mov_b64_e32 v[38:39], 0
	v_mov_b64_e32 v[40:41], 0
	v_mov_b64_e32 v[42:43], 0
	v_mov_b64_e32 v[44:45], 0
	v_mov_b64_e32 v[46:47], 0
	v_mov_b64_e32 v[48:49], 0
	v_mov_b64_e32 v[50:51], 0
	v_mov_b64_e32 v[52:53], 0
	v_mov_b64_e32 v[54:55], 0
	v_mov_b64_e32 v[56:57], 0
	v_mov_b64_e32 v[58:59], 0
	v_mov_b64_e32 v[60:61], 0
	v_mov_b64_e32 v[62:63], 0
	v_mov_b64_e32 v[64:65], 0
	v_mov_b64_e32 v[66:67], 0
	v_mov_b64_e32 v[68:69], 0
	v_mov_b64_e32 v[70:71], 0
	v_mov_b64_e32 v[72:73], 0
	v_mov_b64_e32 v[74:75], 0
	v_mov_b64_e32 v[76:77], 0
	v_mov_b64_e32 v[78:79], 0
	v_mov_b64_e32 v[80:81], 0
	v_mov_b64_e32 v[82:83], 0
	v_mov_b64_e32 v[84:85], 0
	v_mov_b64_e32 v[86:87], 0
	v_mov_b64_e32 v[88:89], 0
	v_mov_b64_e32 v[90:91], 0
	v_mov_b64_e32 v[92:93], 0
	v_mov_b64_e32 v[94:95], 0
	v_mov_b64_e32 v[96:97], 0
	v_mov_b64_e32 v[98:99], 0
	v_mov_b64_e32 v[100:101], 0
	v_mov_b64_e32 v[102:103], 0
	v_mov_b64_e32 v[104:105], 0
	v_mov_b64_e32 v[106:107], 0
	v_mov_b64_e32 v[108:109], 0
	v_mov_b64_e32 v[110:111], 0
	v_mov_b64_e32 v[112:113], 0
	v_mov_b64_e32 v[114:115], 0
	v_mov_b64_e32 v[116:117], 0
	v_mov_b64_e32 v[118:119], 0
	v_mov_b64_e32 v[120:121], 0
	v_mov_b64_e32 v[122:123], 0
	v_mov_b64_e32 v[124:125], 0
	v_mov_b64_e32 v[126:127], 0
	v_mov_b64_e32 v[128:129], 0

.LBB0_635:
	s_andn2_b64 vcc, exec, s[20:21]
	s_cbranch_vccnz .Lzs_3
	s_add_i32 s28, s79, 0x80
	s_add_i32 s79, s75, 0x100
	s_mov_b32 s80, 0
	v_mov_b64_e32 v[2:3], 0
	v_mov_b64_e32 v[4:5], 0
	v_mov_b64_e32 v[6:7], 0
	v_mov_b64_e32 v[8:9], 0
	v_mov_b64_e32 v[10:11], 0
	v_mov_b64_e32 v[12:13], 0
	v_mov_b64_e32 v[14:15], 0
	v_mov_b64_e32 v[16:17], 0
	v_mov_b64_e32 v[18:19], 0
	v_mov_b64_e32 v[20:21], 0
	v_mov_b64_e32 v[22:23], 0
	v_mov_b64_e32 v[24:25], 0
	v_mov_b64_e32 v[26:27], 0
	v_mov_b64_e32 v[28:29], 0
	v_mov_b64_e32 v[30:31], 0
	v_mov_b64_e32 v[32:33], 0
	v_mov_b64_e32 v[34:35], 0
	v_mov_b64_e32 v[36:37], 0
	v_mov_b64_e32 v[38:39], 0
	v_mov_b64_e32 v[40:41], 0
	v_mov_b64_e32 v[42:43], 0
	v_mov_b64_e32 v[44:45], 0
	v_mov_b64_e32 v[46:47], 0
	v_mov_b64_e32 v[48:49], 0
	v_mov_b64_e32 v[50:51], 0
	v_mov_b64_e32 v[52:53], 0
	v_mov_b64_e32 v[54:55], 0
	v_mov_b64_e32 v[56:57], 0
	v_mov_b64_e32 v[58:59], 0
	v_mov_b64_e32 v[60:61], 0
	v_mov_b64_e32 v[62:63], 0
	v_mov_b64_e32 v[64:65], 0
	v_mov_b64_e32 v[66:67], 0
	v_mov_b64_e32 v[68:69], 0
	v_mov_b64_e32 v[70:71], 0
	v_mov_b64_e32 v[72:73], 0
	v_mov_b64_e32 v[74:75], 0
	v_mov_b64_e32 v[76:77], 0
	v_mov_b64_e32 v[78:79], 0
	v_mov_b64_e32 v[80:81], 0
	v_mov_b64_e32 v[82:83], 0
	v_mov_b64_e32 v[84:85], 0
	v_mov_b64_e32 v[86:87], 0
	v_mov_b64_e32 v[88:89], 0
	v_mov_b64_e32 v[90:91], 0
	v_mov_b64_e32 v[92:93], 0
	v_mov_b64_e32 v[94:95], 0
	v_mov_b64_e32 v[96:97], 0
	v_mov_b64_e32 v[98:99], 0
	v_mov_b64_e32 v[100:101], 0
	v_mov_b64_e32 v[102:103], 0
	v_mov_b64_e32 v[104:105], 0
	v_mov_b64_e32 v[106:107], 0
	v_mov_b64_e32 v[108:109], 0
	v_mov_b64_e32 v[110:111], 0
	v_mov_b64_e32 v[112:113], 0
	v_mov_b64_e32 v[114:115], 0
	v_mov_b64_e32 v[116:117], 0
	v_mov_b64_e32 v[118:119], 0
	v_mov_b64_e32 v[120:121], 0
	v_mov_b64_e32 v[122:123], 0
	v_mov_b64_e32 v[124:125], 0
	v_mov_b64_e32 v[126:127], 0
	v_mov_b64_e32 v[128:129], 0

.Lzs_4:
	v_mov_b64_e32 v[2:3], 0
	v_mov_b64_e32 v[4:5], 0
	v_mov_b64_e32 v[6:7], 0
	v_mov_b64_e32 v[8:9], 0
	v_mov_b64_e32 v[10:11], 0
	v_mov_b64_e32 v[12:13], 0
	v_mov_b64_e32 v[14:15], 0
	v_mov_b64_e32 v[16:17], 0
	v_mov_b64_e32 v[18:19], 0
	v_mov_b64_e32 v[20:21], 0
	v_mov_b64_e32 v[22:23], 0
	v_mov_b64_e32 v[24:25], 0
	v_mov_b64_e32 v[26:27], 0
	v_mov_b64_e32 v[28:29], 0
	v_mov_b64_e32 v[30:31], 0
	v_mov_b64_e32 v[32:33], 0
	v_mov_b64_e32 v[34:35], 0
	v_mov_b64_e32 v[36:37], 0
	v_mov_b64_e32 v[38:39], 0
	v_mov_b64_e32 v[40:41], 0
	v_mov_b64_e32 v[42:43], 0
	v_mov_b64_e32 v[44:45], 0
	v_mov_b64_e32 v[46:47], 0
	v_mov_b64_e32 v[48:49], 0
	v_mov_b64_e32 v[50:51], 0
	v_mov_b64_e32 v[52:53], 0
	v_mov_b64_e32 v[54:55], 0
	v_mov_b64_e32 v[56:57], 0
	v_mov_b64_e32 v[58:59], 0
	v_mov_b64_e32 v[60:61], 0
	v_mov_b64_e32 v[62:63], 0
	v_mov_b64_e32 v[64:65], 0
	v_mov_b64_e32 v[66:67], 0
	v_mov_b64_e32 v[68:69], 0
	v_mov_b64_e32 v[70:71], 0
	v_mov_b64_e32 v[72:73], 0
	v_mov_b64_e32 v[74:75], 0
	v_mov_b64_e32 v[76:77], 0
	v_mov_b64_e32 v[78:79], 0
	v_mov_b64_e32 v[80:81], 0
	v_mov_b64_e32 v[82:83], 0
	v_mov_b64_e32 v[84:85], 0
	v_mov_b64_e32 v[86:87], 0
	v_mov_b64_e32 v[88:89], 0
	v_mov_b64_e32 v[90:91], 0
	v_mov_b64_e32 v[92:93], 0
	v_mov_b64_e32 v[94:95], 0
	v_mov_b64_e32 v[96:97], 0
	v_mov_b64_e32 v[98:99], 0
	v_mov_b64_e32 v[100:101], 0
	v_mov_b64_e32 v[102:103], 0
	v_mov_b64_e32 v[104:105], 0
	v_mov_b64_e32 v[106:107], 0
	v_mov_b64_e32 v[108:109], 0
	v_mov_b64_e32 v[110:111], 0
	v_mov_b64_e32 v[112:113], 0
	v_mov_b64_e32 v[130:131], 0
	v_mov_b64_e32 v[132:133], 0
	v_mov_b64_e32 v[134:135], 0
	v_mov_b64_e32 v[136:137], 0
	v_mov_b64_e32 v[138:139], 0
	v_mov_b64_e32 v[140:141], 0
	v_mov_b64_e32 v[142:143], 0
	v_mov_b64_e32 v[144:145], 0
	s_branch .LBB0_1184

.LBB0_1181:
	s_andn2_b64 vcc, exec, s[16:17]
	s_waitcnt lgkmcnt(0)
	s_cbranch_vccnz .Lzs_4
	s_add_i32 s6, s58, 0x80
	s_add_i32 s58, s59, 0x100
	s_mov_b32 s59, 0
	v_mov_b64_e32 v[2:3], 0
	v_mov_b64_e32 v[4:5], 0
	v_mov_b64_e32 v[6:7], 0
	v_mov_b64_e32 v[8:9], 0
	v_mov_b64_e32 v[10:11], 0
	v_mov_b64_e32 v[12:13], 0
	v_mov_b64_e32 v[14:15], 0
	v_mov_b64_e32 v[16:17], 0
	v_mov_b64_e32 v[18:19], 0
	v_mov_b64_e32 v[20:21], 0
	v_mov_b64_e32 v[22:23], 0
	v_mov_b64_e32 v[24:25], 0
	v_mov_b64_e32 v[26:27], 0
	v_mov_b64_e32 v[28:29], 0
	v_mov_b64_e32 v[30:31], 0
	v_mov_b64_e32 v[32:33], 0
	v_mov_b64_e32 v[34:35], 0
	v_mov_b64_e32 v[36:37], 0
	v_mov_b64_e32 v[38:39], 0
	v_mov_b64_e32 v[40:41], 0
	v_mov_b64_e32 v[42:43], 0
	v_mov_b64_e32 v[44:45], 0
	v_mov_b64_e32 v[46:47], 0
	v_mov_b64_e32 v[48:49], 0
	v_mov_b64_e32 v[50:51], 0
	v_mov_b64_e32 v[52:53], 0
	v_mov_b64_e32 v[54:55], 0
	v_mov_b64_e32 v[56:57], 0
	v_mov_b64_e32 v[58:59], 0
	v_mov_b64_e32 v[60:61], 0
	v_mov_b64_e32 v[62:63], 0
	v_mov_b64_e32 v[64:65], 0
	v_mov_b64_e32 v[66:67], 0
	v_mov_b64_e32 v[68:69], 0
	v_mov_b64_e32 v[70:71], 0
	v_mov_b64_e32 v[72:73], 0
	v_mov_b64_e32 v[74:75], 0
	v_mov_b64_e32 v[76:77], 0
	v_mov_b64_e32 v[78:79], 0
	v_mov_b64_e32 v[80:81], 0
	v_mov_b64_e32 v[82:83], 0
	v_mov_b64_e32 v[84:85], 0
	v_mov_b64_e32 v[86:87], 0
	v_mov_b64_e32 v[88:89], 0
	v_mov_b64_e32 v[90:91], 0
	v_mov_b64_e32 v[92:93], 0
	v_mov_b64_e32 v[94:95], 0
	v_mov_b64_e32 v[96:97], 0
	v_mov_b64_e32 v[98:99], 0
	v_mov_b64_e32 v[100:101], 0
	v_mov_b64_e32 v[102:103], 0
	v_mov_b64_e32 v[104:105], 0
	v_mov_b64_e32 v[106:107], 0
	v_mov_b64_e32 v[108:109], 0
	v_mov_b64_e32 v[110:111], 0
	v_mov_b64_e32 v[112:113], 0
	v_mov_b64_e32 v[130:131], 0
	v_mov_b64_e32 v[132:133], 0
	v_mov_b64_e32 v[134:135], 0
	v_mov_b64_e32 v[136:137], 0
	v_mov_b64_e32 v[138:139], 0
	v_mov_b64_e32 v[140:141], 0
	v_mov_b64_e32 v[142:143], 0
	v_mov_b64_e32 v[144:145], 0

.Lzs_5:
	v_mov_b64_e32 v[34:35], 0
	v_mov_b64_e32 v[36:37], 0
	v_mov_b64_e32 v[38:39], 0
	v_mov_b64_e32 v[40:41], 0
	v_mov_b64_e32 v[42:43], 0
	v_mov_b64_e32 v[44:45], 0
	v_mov_b64_e32 v[46:47], 0
	v_mov_b64_e32 v[48:49], 0
	v_mov_b64_e32 v[50:51], 0
	v_mov_b64_e32 v[52:53], 0
	v_mov_b64_e32 v[54:55], 0
	v_mov_b64_e32 v[56:57], 0
	v_mov_b64_e32 v[58:59], 0
	v_mov_b64_e32 v[60:61], 0
	v_mov_b64_e32 v[62:63], 0
	v_mov_b64_e32 v[64:65], 0
	v_mov_b64_e32 v[66:67], 0
	v_mov_b64_e32 v[68:69], 0
	v_mov_b64_e32 v[70:71], 0
	v_mov_b64_e32 v[72:73], 0
	v_mov_b64_e32 v[74:75], 0
	v_mov_b64_e32 v[76:77], 0
	v_mov_b64_e32 v[78:79], 0
	v_mov_b64_e32 v[80:81], 0
	v_mov_b64_e32 v[82:83], 0
	v_mov_b64_e32 v[84:85], 0
	v_mov_b64_e32 v[86:87], 0
	v_mov_b64_e32 v[88:89], 0
	v_mov_b64_e32 v[90:91], 0
	v_mov_b64_e32 v[92:93], 0
	v_mov_b64_e32 v[94:95], 0
	v_mov_b64_e32 v[96:97], 0
	v_mov_b64_e32 v[98:99], 0
	v_mov_b64_e32 v[100:101], 0
	v_mov_b64_e32 v[102:103], 0
	v_mov_b64_e32 v[104:105], 0
	v_mov_b64_e32 v[106:107], 0
	v_mov_b64_e32 v[108:109], 0
	v_mov_b64_e32 v[110:111], 0
	v_mov_b64_e32 v[112:113], 0
	v_mov_b64_e32 v[114:115], 0
	v_mov_b64_e32 v[116:117], 0
	v_mov_b64_e32 v[118:119], 0
	v_mov_b64_e32 v[120:121], 0
	v_mov_b64_e32 v[122:123], 0
	v_mov_b64_e32 v[124:125], 0
	v_mov_b64_e32 v[126:127], 0
	v_mov_b64_e32 v[128:129], 0
	v_mov_b64_e32 v[130:131], 0
	v_mov_b64_e32 v[132:133], 0
	v_mov_b64_e32 v[134:135], 0
	v_mov_b64_e32 v[136:137], 0
	v_mov_b64_e32 v[138:139], 0
	v_mov_b64_e32 v[140:141], 0
	v_mov_b64_e32 v[142:143], 0
	v_mov_b64_e32 v[144:145], 0
	v_mov_b64_e32 v[146:147], 0
	v_mov_b64_e32 v[148:149], 0
	v_mov_b64_e32 v[150:151], 0
	v_mov_b64_e32 v[152:153], 0
	v_mov_b64_e32 v[154:155], 0
	v_mov_b64_e32 v[156:157], 0
	v_mov_b64_e32 v[158:159], 0
	v_mov_b64_e32 v[160:161], 0
	s_branch .LBB0_1604

.LBB0_1601:
	s_andn2_b64 vcc, exec, s[12:13]
	s_cbranch_vccnz .Lzs_5
	s_add_i32 s6, s61, 0x80
	s_add_i32 s61, s62, 0x100
	s_mov_b32 s62, 0
	v_mov_b64_e32 v[34:35], 0
	v_mov_b64_e32 v[36:37], 0
	v_mov_b64_e32 v[38:39], 0
	v_mov_b64_e32 v[40:41], 0
	v_mov_b64_e32 v[42:43], 0
	v_mov_b64_e32 v[44:45], 0
	v_mov_b64_e32 v[46:47], 0
	v_mov_b64_e32 v[48:49], 0
	v_mov_b64_e32 v[50:51], 0
	v_mov_b64_e32 v[52:53], 0
	v_mov_b64_e32 v[54:55], 0
	v_mov_b64_e32 v[56:57], 0
	v_mov_b64_e32 v[58:59], 0
	v_mov_b64_e32 v[60:61], 0
	v_mov_b64_e32 v[62:63], 0
	v_mov_b64_e32 v[64:65], 0
	v_mov_b64_e32 v[66:67], 0
	v_mov_b64_e32 v[68:69], 0
	v_mov_b64_e32 v[70:71], 0
	v_mov_b64_e32 v[72:73], 0
	v_mov_b64_e32 v[74:75], 0
	v_mov_b64_e32 v[76:77], 0
	v_mov_b64_e32 v[78:79], 0
	v_mov_b64_e32 v[80:81], 0
	v_mov_b64_e32 v[82:83], 0
	v_mov_b64_e32 v[84:85], 0
	v_mov_b64_e32 v[86:87], 0
	v_mov_b64_e32 v[88:89], 0
	v_mov_b64_e32 v[90:91], 0
	v_mov_b64_e32 v[92:93], 0
	v_mov_b64_e32 v[94:95], 0
	v_mov_b64_e32 v[96:97], 0
	v_mov_b64_e32 v[98:99], 0
	v_mov_b64_e32 v[100:101], 0
	v_mov_b64_e32 v[102:103], 0
	v_mov_b64_e32 v[104:105], 0
	v_mov_b64_e32 v[106:107], 0
	v_mov_b64_e32 v[108:109], 0
	v_mov_b64_e32 v[110:111], 0
	v_mov_b64_e32 v[112:113], 0
	v_mov_b64_e32 v[114:115], 0
	v_mov_b64_e32 v[116:117], 0
	v_mov_b64_e32 v[118:119], 0
	v_mov_b64_e32 v[120:121], 0
	v_mov_b64_e32 v[122:123], 0
	v_mov_b64_e32 v[124:125], 0
	v_mov_b64_e32 v[126:127], 0
	v_mov_b64_e32 v[128:129], 0
	v_mov_b64_e32 v[130:131], 0
	v_mov_b64_e32 v[132:133], 0
	v_mov_b64_e32 v[134:135], 0
	v_mov_b64_e32 v[136:137], 0
	v_mov_b64_e32 v[138:139], 0
	v_mov_b64_e32 v[140:141], 0
	v_mov_b64_e32 v[142:143], 0
	v_mov_b64_e32 v[144:145], 0
	v_mov_b64_e32 v[146:147], 0
	v_mov_b64_e32 v[148:149], 0
	v_mov_b64_e32 v[150:151], 0
	v_mov_b64_e32 v[152:153], 0
	v_mov_b64_e32 v[154:155], 0
	v_mov_b64_e32 v[156:157], 0
	v_mov_b64_e32 v[158:159], 0
	v_mov_b64_e32 v[160:161], 0

.LBB0_2045:
	s_andn2_b64 vcc, exec, s[16:17]
	s_cbranch_vccnz .Lzs_6
	s_add_i32 s30, s48, 0x100
	s_mov_b32 s48, 0
	v_mov_b64_e32 v[2:3], 0
	v_mov_b64_e32 v[4:5], 0
	v_mov_b64_e32 v[6:7], 0
	v_mov_b64_e32 v[8:9], 0
	v_mov_b64_e32 v[10:11], 0
	v_mov_b64_e32 v[12:13], 0
	v_mov_b64_e32 v[14:15], 0
	v_mov_b64_e32 v[16:17], 0
	v_mov_b64_e32 v[18:19], 0
	v_mov_b64_e32 v[20:21], 0
	v_mov_b64_e32 v[22:23], 0
	v_mov_b64_e32 v[24:25], 0
	v_mov_b64_e32 v[26:27], 0
	v_mov_b64_e32 v[28:29], 0
	v_mov_b64_e32 v[30:31], 0
	v_mov_b64_e32 v[32:33], 0
	v_mov_b64_e32 v[34:35], 0
	v_mov_b64_e32 v[36:37], 0
	v_mov_b64_e32 v[38:39], 0
	v_mov_b64_e32 v[40:41], 0
	v_mov_b64_e32 v[42:43], 0
	v_mov_b64_e32 v[44:45], 0
	v_mov_b64_e32 v[46:47], 0
	v_mov_b64_e32 v[48:49], 0
	v_mov_b64_e32 v[50:51], 0
	v_mov_b64_e32 v[52:53], 0
	v_mov_b64_e32 v[54:55], 0
	v_mov_b64_e32 v[56:57], 0
	v_mov_b64_e32 v[58:59], 0
	v_mov_b64_e32 v[60:61], 0
	v_mov_b64_e32 v[62:63], 0
	v_mov_b64_e32 v[64:65], 0
	v_mov_b64_e32 v[66:67], 0
	v_mov_b64_e32 v[68:69], 0
	v_mov_b64_e32 v[70:71], 0
	v_mov_b64_e32 v[72:73], 0
	v_mov_b64_e32 v[74:75], 0
	v_mov_b64_e32 v[76:77], 0
	v_mov_b64_e32 v[78:79], 0
	v_mov_b64_e32 v[80:81], 0
	v_mov_b64_e32 v[82:83], 0
	v_mov_b64_e32 v[84:85], 0
	v_mov_b64_e32 v[86:87], 0
	v_mov_b64_e32 v[88:89], 0
	v_mov_b64_e32 v[90:91], 0
	v_mov_b64_e32 v[92:93], 0
	v_mov_b64_e32 v[94:95], 0
	v_mov_b64_e32 v[96:97], 0
	v_mov_b64_e32 v[98:99], 0
	v_mov_b64_e32 v[100:101], 0
	v_mov_b64_e32 v[102:103], 0
	v_mov_b64_e32 v[104:105], 0
	v_mov_b64_e32 v[106:107], 0
	v_mov_b64_e32 v[108:109], 0
	v_mov_b64_e32 v[110:111], 0
	v_mov_b64_e32 v[112:113], 0
	v_mov_b64_e32 v[114:115], 0
	v_mov_b64_e32 v[116:117], 0
	v_mov_b64_e32 v[118:119], 0
	v_mov_b64_e32 v[120:121], 0
	v_mov_b64_e32 v[122:123], 0
	v_mov_b64_e32 v[124:125], 0
	v_mov_b64_e32 v[126:127], 0
	v_mov_b64_e32 v[128:129], 0

.LBB0_2335:
	s_andn2_b64 vcc, exec, s[14:15]
	s_cbranch_vccnz .Lzs_7
	s_add_i32 s50, s87, 0x80
	s_add_i32 s87, s75, 0x100
	s_mov_b32 s88, 0
	v_mov_b64_e32 v[2:3], 0
	v_mov_b64_e32 v[4:5], 0
	v_mov_b64_e32 v[6:7], 0
	v_mov_b64_e32 v[8:9], 0
	v_mov_b64_e32 v[10:11], 0
	v_mov_b64_e32 v[12:13], 0
	v_mov_b64_e32 v[14:15], 0
	v_mov_b64_e32 v[16:17], 0
	v_mov_b64_e32 v[18:19], 0
	v_mov_b64_e32 v[20:21], 0
	v_mov_b64_e32 v[22:23], 0
	v_mov_b64_e32 v[24:25], 0
	v_mov_b64_e32 v[26:27], 0
	v_mov_b64_e32 v[28:29], 0
	v_mov_b64_e32 v[30:31], 0
	v_mov_b64_e32 v[32:33], 0
	v_mov_b64_e32 v[34:35], 0
	v_mov_b64_e32 v[36:37], 0
	v_mov_b64_e32 v[38:39], 0
	v_mov_b64_e32 v[40:41], 0
	v_mov_b64_e32 v[42:43], 0
	v_mov_b64_e32 v[44:45], 0
	v_mov_b64_e32 v[46:47], 0
	v_mov_b64_e32 v[48:49], 0
	v_mov_b64_e32 v[50:51], 0
	v_mov_b64_e32 v[52:53], 0
	v_mov_b64_e32 v[54:55], 0
	v_mov_b64_e32 v[56:57], 0
	v_mov_b64_e32 v[58:59], 0
	v_mov_b64_e32 v[60:61], 0
	v_mov_b64_e32 v[62:63], 0
	v_mov_b64_e32 v[64:65], 0
	v_mov_b64_e32 v[66:67], 0
	v_mov_b64_e32 v[68:69], 0
	v_mov_b64_e32 v[70:71], 0
	v_mov_b64_e32 v[72:73], 0
	v_mov_b64_e32 v[74:75], 0
	v_mov_b64_e32 v[76:77], 0
	v_mov_b64_e32 v[78:79], 0
	v_mov_b64_e32 v[80:81], 0
	v_mov_b64_e32 v[82:83], 0
	v_mov_b64_e32 v[84:85], 0
	v_mov_b64_e32 v[86:87], 0
	v_mov_b64_e32 v[88:89], 0
	v_mov_b64_e32 v[90:91], 0
	v_mov_b64_e32 v[92:93], 0
	v_mov_b64_e32 v[94:95], 0
	v_mov_b64_e32 v[96:97], 0
	v_mov_b64_e32 v[98:99], 0
	v_mov_b64_e32 v[100:101], 0
	v_mov_b64_e32 v[102:103], 0
	v_mov_b64_e32 v[104:105], 0
	v_mov_b64_e32 v[106:107], 0
	v_mov_b64_e32 v[108:109], 0
	v_mov_b64_e32 v[110:111], 0
	v_mov_b64_e32 v[112:113], 0
	v_mov_b64_e32 v[114:115], 0
	v_mov_b64_e32 v[116:117], 0
	v_mov_b64_e32 v[118:119], 0
	v_mov_b64_e32 v[120:121], 0
	v_mov_b64_e32 v[122:123], 0
	v_mov_b64_e32 v[124:125], 0
	v_mov_b64_e32 v[126:127], 0
	v_mov_b64_e32 v[128:129], 0

.Lzs_8:
	v_mov_b64_e32 v[2:3], 0
	v_mov_b64_e32 v[4:5], 0
	v_mov_b64_e32 v[6:7], 0
	v_mov_b64_e32 v[8:9], 0
	v_mov_b64_e32 v[10:11], 0
	v_mov_b64_e32 v[12:13], 0
	v_mov_b64_e32 v[14:15], 0
	v_mov_b64_e32 v[16:17], 0
	v_mov_b64_e32 v[18:19], 0
	v_mov_b64_e32 v[20:21], 0
	v_mov_b64_e32 v[22:23], 0
	v_mov_b64_e32 v[24:25], 0
	v_mov_b64_e32 v[26:27], 0
	v_mov_b64_e32 v[28:29], 0
	v_mov_b64_e32 v[30:31], 0
	v_mov_b64_e32 v[32:33], 0
	v_mov_b64_e32 v[34:35], 0
	v_mov_b64_e32 v[36:37], 0
	v_mov_b64_e32 v[38:39], 0
	v_mov_b64_e32 v[40:41], 0
	v_mov_b64_e32 v[42:43], 0
	v_mov_b64_e32 v[44:45], 0
	v_mov_b64_e32 v[46:47], 0
	v_mov_b64_e32 v[48:49], 0
	v_mov_b64_e32 v[50:51], 0
	v_mov_b64_e32 v[52:53], 0
	v_mov_b64_e32 v[54:55], 0
	v_mov_b64_e32 v[56:57], 0
	v_mov_b64_e32 v[58:59], 0
	v_mov_b64_e32 v[60:61], 0
	v_mov_b64_e32 v[62:63], 0
	v_mov_b64_e32 v[64:65], 0
	v_mov_b64_e32 v[66:67], 0
	v_mov_b64_e32 v[68:69], 0
	v_mov_b64_e32 v[70:71], 0
	v_mov_b64_e32 v[72:73], 0
	v_mov_b64_e32 v[74:75], 0
	v_mov_b64_e32 v[76:77], 0
	v_mov_b64_e32 v[78:79], 0
	v_mov_b64_e32 v[80:81], 0
	v_mov_b64_e32 v[82:83], 0
	v_mov_b64_e32 v[84:85], 0
	v_mov_b64_e32 v[86:87], 0
	v_mov_b64_e32 v[88:89], 0
	v_mov_b64_e32 v[98:99], 0
	v_mov_b64_e32 v[100:101], 0
	v_mov_b64_e32 v[102:103], 0
	v_mov_b64_e32 v[104:105], 0
	v_mov_b64_e32 v[106:107], 0
	v_mov_b64_e32 v[108:109], 0
	v_mov_b64_e32 v[110:111], 0
	v_mov_b64_e32 v[112:113], 0
	v_mov_b64_e32 v[114:115], 0
	v_mov_b64_e32 v[116:117], 0
	v_mov_b64_e32 v[118:119], 0
	v_mov_b64_e32 v[120:121], 0
	v_mov_b64_e32 v[122:123], 0
	v_mov_b64_e32 v[124:125], 0
	v_mov_b64_e32 v[126:127], 0
	v_mov_b64_e32 v[128:129], 0
	v_mov_b64_e32 v[130:131], 0
	v_mov_b64_e32 v[132:133], 0
	v_mov_b64_e32 v[134:135], 0
	v_mov_b64_e32 v[136:137], 0
	s_branch .LBB0_2522

.LBB0_2519:
	s_andn2_b64 vcc, exec, s[14:15]
	s_cbranch_vccnz .Lzs_8
	s_add_i32 s56, s96, 0x80
	s_add_i32 s57, s74, 0x100
	s_mov_b32 s74, 0
	v_mov_b64_e32 v[2:3], 0
	v_mov_b64_e32 v[4:5], 0
	v_mov_b64_e32 v[6:7], 0
	v_mov_b64_e32 v[8:9], 0
	v_mov_b64_e32 v[10:11], 0
	v_mov_b64_e32 v[12:13], 0
	v_mov_b64_e32 v[14:15], 0
	v_mov_b64_e32 v[16:17], 0
	v_mov_b64_e32 v[18:19], 0
	v_mov_b64_e32 v[20:21], 0
	v_mov_b64_e32 v[22:23], 0
	v_mov_b64_e32 v[24:25], 0
	v_mov_b64_e32 v[26:27], 0
	v_mov_b64_e32 v[28:29], 0
	v_mov_b64_e32 v[30:31], 0
	v_mov_b64_e32 v[32:33], 0
	v_mov_b64_e32 v[34:35], 0
	v_mov_b64_e32 v[36:37], 0
	v_mov_b64_e32 v[38:39], 0
	v_mov_b64_e32 v[40:41], 0
	v_mov_b64_e32 v[42:43], 0
	v_mov_b64_e32 v[44:45], 0
	v_mov_b64_e32 v[46:47], 0
	v_mov_b64_e32 v[48:49], 0
	v_mov_b64_e32 v[50:51], 0
	v_mov_b64_e32 v[52:53], 0
	v_mov_b64_e32 v[54:55], 0
	v_mov_b64_e32 v[56:57], 0
	v_mov_b64_e32 v[58:59], 0
	v_mov_b64_e32 v[60:61], 0
	v_mov_b64_e32 v[62:63], 0
	v_mov_b64_e32 v[64:65], 0
	v_mov_b64_e32 v[66:67], 0
	v_mov_b64_e32 v[68:69], 0
	v_mov_b64_e32 v[70:71], 0
	v_mov_b64_e32 v[72:73], 0
	v_mov_b64_e32 v[74:75], 0
	v_mov_b64_e32 v[76:77], 0
	v_mov_b64_e32 v[78:79], 0
	v_mov_b64_e32 v[80:81], 0
	v_mov_b64_e32 v[82:83], 0
	v_mov_b64_e32 v[84:85], 0
	v_mov_b64_e32 v[86:87], 0
	v_mov_b64_e32 v[88:89], 0
	v_mov_b64_e32 v[98:99], 0
	v_mov_b64_e32 v[100:101], 0
	v_mov_b64_e32 v[102:103], 0
	v_mov_b64_e32 v[104:105], 0
	v_mov_b64_e32 v[106:107], 0
	v_mov_b64_e32 v[108:109], 0
	v_mov_b64_e32 v[110:111], 0
	v_mov_b64_e32 v[112:113], 0
	v_mov_b64_e32 v[114:115], 0
	v_mov_b64_e32 v[116:117], 0
	v_mov_b64_e32 v[118:119], 0
	v_mov_b64_e32 v[120:121], 0
	v_mov_b64_e32 v[122:123], 0
	v_mov_b64_e32 v[124:125], 0
	v_mov_b64_e32 v[126:127], 0
	v_mov_b64_e32 v[128:129], 0
	v_mov_b64_e32 v[130:131], 0
	v_mov_b64_e32 v[132:133], 0
	v_mov_b64_e32 v[134:135], 0
	v_mov_b64_e32 v[136:137], 0

.LBB0_2595:
	s_andn2_b64 vcc, exec, s[12:13]
	s_cbranch_vccnz .Lzs_9
	s_add_i32 s60, s64, 0x80
	s_addk_i32 s63, 0x100
	s_mov_b32 s64, 0
	v_mov_b64_e32 v[2:3], 0
	v_mov_b64_e32 v[4:5], 0
	v_mov_b64_e32 v[6:7], 0
	v_mov_b64_e32 v[8:9], 0
	v_mov_b64_e32 v[10:11], 0
	v_mov_b64_e32 v[12:13], 0
	v_mov_b64_e32 v[14:15], 0
	v_mov_b64_e32 v[16:17], 0
	v_mov_b64_e32 v[18:19], 0
	v_mov_b64_e32 v[20:21], 0
	v_mov_b64_e32 v[22:23], 0
	v_mov_b64_e32 v[24:25], 0
	v_mov_b64_e32 v[26:27], 0
	v_mov_b64_e32 v[28:29], 0
	v_mov_b64_e32 v[30:31], 0
	v_mov_b64_e32 v[32:33], 0
	v_mov_b64_e32 v[34:35], 0
	v_mov_b64_e32 v[36:37], 0
	v_mov_b64_e32 v[38:39], 0
	v_mov_b64_e32 v[40:41], 0
	v_mov_b64_e32 v[42:43], 0
	v_mov_b64_e32 v[44:45], 0
	v_mov_b64_e32 v[46:47], 0
	v_mov_b64_e32 v[48:49], 0
	v_mov_b64_e32 v[50:51], 0
	v_mov_b64_e32 v[52:53], 0
	v_mov_b64_e32 v[54:55], 0
	v_mov_b64_e32 v[56:57], 0
	v_mov_b64_e32 v[58:59], 0
	v_mov_b64_e32 v[60:61], 0
	v_mov_b64_e32 v[62:63], 0
	v_mov_b64_e32 v[64:65], 0
	v_mov_b64_e32 v[66:67], 0
	v_mov_b64_e32 v[68:69], 0
	v_mov_b64_e32 v[70:71], 0
	v_mov_b64_e32 v[72:73], 0
	v_mov_b64_e32 v[74:75], 0
	v_mov_b64_e32 v[76:77], 0
	v_mov_b64_e32 v[78:79], 0
	v_mov_b64_e32 v[80:81], 0
	v_mov_b64_e32 v[82:83], 0
	v_mov_b64_e32 v[84:85], 0
	v_mov_b64_e32 v[86:87], 0
	v_mov_b64_e32 v[88:89], 0
	v_mov_b64_e32 v[90:91], 0
	v_mov_b64_e32 v[92:93], 0
	v_mov_b64_e32 v[94:95], 0
	v_mov_b64_e32 v[96:97], 0
	v_mov_b64_e32 v[98:99], 0
	v_mov_b64_e32 v[100:101], 0
	v_mov_b64_e32 v[102:103], 0
	v_mov_b64_e32 v[104:105], 0
	v_mov_b64_e32 v[106:107], 0
	v_mov_b64_e32 v[108:109], 0
	v_mov_b64_e32 v[110:111], 0
	v_mov_b64_e32 v[112:113], 0
	v_mov_b64_e32 v[114:115], 0
	v_mov_b64_e32 v[116:117], 0
	v_mov_b64_e32 v[118:119], 0
	v_mov_b64_e32 v[120:121], 0
	v_mov_b64_e32 v[122:123], 0
	v_mov_b64_e32 v[124:125], 0
	v_mov_b64_e32 v[126:127], 0
	v_mov_b64_e32 v[128:129], 0

.Lzs_10:
	v_mov_b64_e32 v[2:3], 0
	v_mov_b64_e32 v[4:5], 0
	v_mov_b64_e32 v[6:7], 0
	v_mov_b64_e32 v[8:9], 0
	v_mov_b64_e32 v[10:11], 0
	v_mov_b64_e32 v[12:13], 0
	v_mov_b64_e32 v[14:15], 0
	v_mov_b64_e32 v[16:17], 0
	v_mov_b64_e32 v[18:19], 0
	v_mov_b64_e32 v[20:21], 0
	v_mov_b64_e32 v[22:23], 0
	v_mov_b64_e32 v[24:25], 0
	v_mov_b64_e32 v[26:27], 0
	v_mov_b64_e32 v[28:29], 0
	v_mov_b64_e32 v[30:31], 0
	v_mov_b64_e32 v[32:33], 0
	v_mov_b64_e32 v[46:47], 0
	v_mov_b64_e32 v[54:55], 0
	v_mov_b64_e32 v[56:57], 0
	v_mov_b64_e32 v[62:63], 0
	v_mov_b64_e32 v[64:65], 0
	v_mov_b64_e32 v[70:71], 0
	v_mov_b64_e32 v[72:73], 0
	v_mov_b64_e32 v[78:79], 0
	v_mov_b64_e32 v[80:81], 0
	v_mov_b64_e32 v[90:91], 0
	v_mov_b64_e32 v[92:93], 0
	v_mov_b64_e32 v[94:95], 0
	v_mov_b64_e32 v[96:97], 0
	v_mov_b64_e32 v[98:99], 0
	v_mov_b64_e32 v[100:101], 0
	v_mov_b64_e32 v[102:103], 0
	v_mov_b64_e32 v[104:105], 0
	v_mov_b64_e32 v[106:107], 0
	v_mov_b64_e32 v[108:109], 0
	v_mov_b64_e32 v[110:111], 0
	v_mov_b64_e32 v[112:113], 0
	v_mov_b64_e32 v[118:119], 0
	v_mov_b64_e32 v[120:121], 0
	v_mov_b64_e32 v[122:123], 0
	v_mov_b64_e32 v[126:127], 0
	v_mov_b64_e32 v[128:129], 0
	v_mov_b64_e32 v[130:131], 0
	v_mov_b64_e32 v[132:133], 0
	v_mov_b64_e32 v[134:135], 0
	v_mov_b64_e32 v[136:137], 0
	v_mov_b64_e32 v[138:139], 0
	v_mov_b64_e32 v[140:141], 0
	v_mov_b64_e32 v[142:143], 0
	v_mov_b64_e32 v[144:145], 0
	v_mov_b64_e32 v[146:147], 0
	v_mov_b64_e32 v[148:149], 0
	v_mov_b64_e32 v[150:151], 0
	v_mov_b64_e32 v[152:153], 0
	v_mov_b64_e32 v[154:155], 0
	v_mov_b64_e32 v[156:157], 0
	v_mov_b64_e32 v[158:159], 0
	v_mov_b64_e32 v[160:161], 0
	v_mov_b64_e32 v[164:165], 0
	v_mov_b64_e32 v[166:167], 0
	v_mov_b64_e32 v[168:169], 0
	v_mov_b64_e32 v[170:171], 0
	v_mov_b64_e32 v[172:173], 0
	v_mov_b64_e32 v[174:175], 0
	s_branch .LBB0_2939

.LBB0_2934:
	s_ashr_i32 s22, s25, 3
	s_add_i32 s22, s29, s22
	s_mul_hi_i32 s23, s22, 0x2e8ba2e9
	s_lshr_b32 s25, s23, 31
	s_ashr_i32 s23, s23, 6
	s_add_i32 s23, s23, s25
	s_lshl_b32 s25, s23, 3
	s_sub_i32 s28, s19, s25
	s_min_i32 s28, s28, 8
	s_abs_i32 s29, s28
	v_cvt_f32_u32_e32 v2, s29
	s_sub_i32 s80, 0, s29
	s_mulk_i32 s23, 0x160
	s_sub_i32 s22, s22, s23
	v_rcp_iflag_f32_e32 v2, v2
	s_abs_i32 s23, s22
	s_xor_b32 s79, s22, s28
	s_ashr_i32 s79, s79, 31
	v_mul_f32_e32 v2, 0x4f7ffffe, v2
	v_cvt_u32_f32_e32 v2, v2
	s_nop 0
	v_readfirstlane_b32 s84, v2
	s_mul_i32 s80, s80, s84
	s_mul_hi_u32 s80, s84, s80
	s_add_i32 s84, s84, s80
	s_mul_hi_u32 s80, s23, s84
	s_mul_i32 s84, s80, s29
	s_sub_i32 s23, s23, s84
	s_add_i32 s85, s80, 1
	s_sub_i32 s84, s23, s29
	s_cmp_ge_u32 s23, s29
	s_cselect_b32 s80, s85, s80
	s_cselect_b32 s23, s84, s23
	s_add_i32 s84, s80, 1
	s_cmp_ge_u32 s23, s29
	s_cselect_b32 s23, s84, s80
	s_xor_b32 s23, s23, s79
	s_sub_i32 s79, s23, s79
	s_mul_i32 s23, s79, s28
	s_sub_i32 s22, s22, s23
	s_add_i32 s22, s25, s22
	s_ashr_i32 s23, s22, 31
	s_lshl_b32 s80, s22, 19
	s_lshl_b64 s[28:29], s[22:23], 2
	s_add_u32 s28, s45, s28
	s_addc_u32 s29, s46, s29
	global_load_dword v230, v1, s[28:29]
	s_mov_b32 s25, s80
.LBB0_2935:
	s_andn2_b64 vcc, exec, s[14:15]
	v_mov_b64_e32 v[2:3], 0
	v_mov_b64_e32 v[4:5], 0
	v_mov_b64_e32 v[6:7], 0
	v_mov_b64_e32 v[8:9], 0
	v_mov_b64_e32 v[10:11], 0
	v_mov_b64_e32 v[12:13], 0
	v_mov_b64_e32 v[14:15], 0
	v_mov_b64_e32 v[16:17], 0
	v_mov_b64_e32 v[18:19], 0
	v_mov_b64_e32 v[20:21], 0
	v_mov_b64_e32 v[22:23], 0
	v_mov_b64_e32 v[24:25], 0
	v_mov_b64_e32 v[26:27], 0
	v_mov_b64_e32 v[28:29], 0
	v_mov_b64_e32 v[30:31], 0
	v_mov_b64_e32 v[32:33], 0
	v_mov_b64_e32 v[164:165], 0
	v_mov_b64_e32 v[166:167], 0
	v_mov_b64_e32 v[168:169], 0
	v_mov_b64_e32 v[170:171], 0
	v_mov_b64_e32 v[172:173], 0
	v_mov_b64_e32 v[174:175], 0
	s_cbranch_vccnz .Lzs_10
	s_add_i32 s28, s82, 0x80
	s_add_i32 s82, s83, 0x100
	s_mov_b32 s83, 0
	v_mov_b64_e32 v[34:35], 0
	v_mov_b64_e32 v[36:37], 0
	v_mov_b64_e32 v[38:39], 0
	v_mov_b64_e32 v[40:41], 0
	v_mov_b64_e32 v[42:43], 0
	v_mov_b64_e32 v[44:45], 0
	v_mov_b64_e32 v[46:47], 0
	v_mov_b64_e32 v[48:49], 0
	v_mov_b64_e32 v[50:51], 0
	v_mov_b64_e32 v[52:53], 0
	v_mov_b64_e32 v[54:55], 0
	v_mov_b64_e32 v[56:57], 0
	v_mov_b64_e32 v[58:59], 0
	v_mov_b64_e32 v[60:61], 0
	v_mov_b64_e32 v[62:63], 0
	v_mov_b64_e32 v[64:65], 0
	v_mov_b64_e32 v[66:67], 0
	v_mov_b64_e32 v[68:69], 0
	v_mov_b64_e32 v[70:71], 0
	v_mov_b64_e32 v[72:73], 0
	v_mov_b64_e32 v[74:75], 0
	v_mov_b64_e32 v[76:77], 0
	v_mov_b64_e32 v[78:79], 0
	v_mov_b64_e32 v[80:81], 0
	v_mov_b64_e32 v[82:83], 0
	v_mov_b64_e32 v[84:85], 0
	v_mov_b64_e32 v[86:87], 0
	v_mov_b64_e32 v[88:89], 0
	v_mov_b64_e32 v[90:91], 0
	v_mov_b64_e32 v[92:93], 0
	v_mov_b64_e32 v[94:95], 0
	v_mov_b64_e32 v[96:97], 0
	v_mov_b64_e32 v[98:99], 0
	v_mov_b64_e32 v[100:101], 0
	v_mov_b64_e32 v[102:103], 0
	v_mov_b64_e32 v[104:105], 0
	v_mov_b64_e32 v[106:107], 0
	v_mov_b64_e32 v[108:109], 0
	v_mov_b64_e32 v[110:111], 0
	v_mov_b64_e32 v[112:113], 0
	v_mov_b64_e32 v[114:115], 0
	v_mov_b64_e32 v[116:117], 0
	v_mov_b64_e32 v[118:119], 0
	v_mov_b64_e32 v[120:121], 0
	v_mov_b64_e32 v[122:123], 0
	v_mov_b64_e32 v[124:125], 0
	v_mov_b64_e32 v[126:127], 0
	v_mov_b64_e32 v[128:129], 0
	v_mov_b64_e32 v[130:131], 0
	v_mov_b64_e32 v[132:133], 0
	v_mov_b64_e32 v[134:135], 0
	v_mov_b64_e32 v[136:137], 0
	v_mov_b64_e32 v[138:139], 0
	v_mov_b64_e32 v[140:141], 0
	v_mov_b64_e32 v[142:143], 0
	v_mov_b64_e32 v[144:145], 0
	v_mov_b64_e32 v[146:147], 0
	v_mov_b64_e32 v[148:149], 0
	v_mov_b64_e32 v[150:151], 0
	v_mov_b64_e32 v[152:153], 0
	v_mov_b64_e32 v[154:155], 0
	v_mov_b64_e32 v[156:157], 0
	v_mov_b64_e32 v[158:159], 0
	v_mov_b64_e32 v[160:161], 0
.LBB0_2937:
	ds_read_b128 v[18:21], v180
	ds_read_b128 v[22:25], v181
	ds_read_b128 v[26:29], v188
	ds_read_b128 v[30:33], v189
	ds_read_b128 v[2:5], v182
	ds_read_b128 v[6:9], v183
	ds_read_b128 v[10:13], v190
	ds_read_b128 v[14:17], v191
	s_add_i32 s84, s28, 0x80
	s_cmp_eq_u32 s67, s83
	s_cselect_b32 s86, s25, s84
	s_cselect_b32 s87, s29, s82
	s_add_i32 s84, s86, 0x80
	s_add_i32 s85, s87, 0x80
	v_mov_b32_e32 v172, v176
	ds_read_b128 v[164:167], v196
	ds_read_b128 v[168:171], v196 offset:1024
	ds_read_b128 v[198:201], v196 offset:2048
	ds_read_b128 v[202:205], v196 offset:3072
	ds_read_b128 v[214:217], v196 offset:4096
	ds_read_b128 v[218:221], v196 offset:5120
	ds_read_b128 v[222:225], v196 offset:6144
	ds_read_b128 v[226:229], v196 offset:7168
	s_add_i32 s88, s28, s65
	v_add_u32_e32 v172, s88, v172
	s_add_i32 m0, s49, 0xc000
	s_add_i32 s88, s28, s70
	global_load_lds_dwordx4 v172, s[4:5]
	v_mov_b32_e32 v172, v176
	s_add_i32 m0, s49, 0xe000
	v_add_u32_e32 v172, s88, v172
	global_load_lds_dwordx4 v172, s[4:5]
	s_waitcnt vmcnt(8)
	s_waitcnt lgkmcnt(0)
	s_barrier
	s_setprio 1
	s_waitcnt lgkmcnt(0)
	v_mfma_f32_16x16x128_f8f6f4 v[158:161], v[18:25], v[164:171], v[158:161]
	v_mfma_f32_16x16x128_f8f6f4 v[154:157], v[26:33], v[164:171], v[154:157]
	v_mfma_f32_16x16x128_f8f6f4 v[150:153], v[18:25], v[198:205], v[150:153]
	v_mfma_f32_16x16x128_f8f6f4 v[146:149], v[26:33], v[198:205], v[146:149]
	v_mfma_f32_16x16x128_f8f6f4 v[138:141], v[18:25], v[214:221], v[138:141]
	v_mfma_f32_16x16x128_f8f6f4 v[130:133], v[26:33], v[214:221], v[130:133]
	v_mfma_f32_16x16x128_f8f6f4 v[122:125], v[18:25], v[222:229], v[122:125]
	v_mfma_f32_16x16x128_f8f6f4 v[114:117], v[26:33], v[222:229], v[114:117]
	s_setprio 0
	s_setprio 1
	v_mfma_f32_16x16x128_f8f6f4 v[142:145], v[2:9], v[164:171], v[142:145]
	v_mfma_f32_16x16x128_f8f6f4 v[134:137], v[10:17], v[164:171], v[134:137]
	v_mfma_f32_16x16x128_f8f6f4 v[126:129], v[2:9], v[198:205], v[126:129]
	v_mfma_f32_16x16x128_f8f6f4 v[118:121], v[10:17], v[198:205], v[118:121]
	v_mfma_f32_16x16x128_f8f6f4 v[110:113], v[2:9], v[214:221], v[110:113]
	v_mfma_f32_16x16x128_f8f6f4 v[106:109], v[10:17], v[214:221], v[106:109]
	v_mfma_f32_16x16x128_f8f6f4 v[102:105], v[2:9], v[222:229], v[102:105]
	v_mfma_f32_16x16x128_f8f6f4 v[98:101], v[10:17], v[222:229], v[98:101]
	s_setprio 0
	s_barrier
	v_mov_b32_e32 v172, v177
	ds_read_b128 v[164:167], v196 offset:16384
	ds_read_b128 v[168:171], v196 offset:17408
	ds_read_b128 v[198:201], v196 offset:18432
	ds_read_b128 v[202:205], v196 offset:19456
	ds_read_b128 v[214:217], v196 offset:20480
	ds_read_b128 v[218:221], v196 offset:21504
	ds_read_b128 v[222:225], v196 offset:22528
	ds_read_b128 v[226:229], v196 offset:23552
	s_mov_b32 m0, s50
	v_add_u32_e32 v172, s87, v172
	global_load_lds_dwordx4 v172, s[6:7]
	v_mov_b32_e32 v172, v177
	s_add_i32 s87, s87, s48
	v_add_u32_e32 v172, s87, v172
	s_mov_b32 m0, s51
	s_add_i32 s87, s87, s48
	global_load_lds_dwordx4 v172, s[6:7]
	v_mov_b32_e32 v172, v177
	s_mov_b32 m0, s52
	v_add_u32_e32 v172, s87, v172
	global_load_lds_dwordx4 v172, s[6:7]
	v_mov_b32_e32 v172, v177
	s_add_i32 s87, s87, s48
	v_add_u32_e32 v172, s87, v172
	s_mov_b32 m0, s53
	s_nop 0
	global_load_lds_dwordx4 v172, s[6:7]
	v_mov_b32_e32 v172, v176
	s_mov_b32 m0, s49
	v_add_u32_e32 v172, s86, v172
	global_load_lds_dwordx4 v172, s[4:5]
	v_mov_b32_e32 v172, v176
	s_add_i32 s86, s86, s47
	v_add_u32_e32 v172, s86, v172
	s_mov_b32 m0, s54
	s_nop 0
	global_load_lds_dwordx4 v172, s[4:5]
	s_waitcnt vmcnt(8)
	s_waitcnt lgkmcnt(0)
	s_barrier
	s_setprio 1
	s_waitcnt lgkmcnt(0)
	v_mfma_f32_16x16x128_f8f6f4 v[94:97], v[18:25], v[164:171], v[94:97]
	v_mfma_f32_16x16x128_f8f6f4 v[90:93], v[26:33], v[164:171], v[90:93]
	v_mfma_f32_16x16x128_f8f6f4 v[86:89], v[18:25], v[198:205], v[86:89]
	v_mfma_f32_16x16x128_f8f6f4 v[82:85], v[26:33], v[198:205], v[82:85]
	v_mfma_f32_16x16x128_f8f6f4 v[74:77], v[18:25], v[214:221], v[74:77]
	v_mfma_f32_16x16x128_f8f6f4 v[66:69], v[26:33], v[214:221], v[66:69]
	v_mfma_f32_16x16x128_f8f6f4 v[58:61], v[18:25], v[222:229], v[58:61]
	v_mfma_f32_16x16x128_f8f6f4 v[50:53], v[26:33], v[222:229], v[50:53]
	s_setprio 0
	s_setprio 1
	v_mfma_f32_16x16x128_f8f6f4 v[78:81], v[2:9], v[164:171], v[78:81]
	v_mfma_f32_16x16x128_f8f6f4 v[70:73], v[10:17], v[164:171], v[70:73]
	v_mfma_f32_16x16x128_f8f6f4 v[62:65], v[2:9], v[198:205], v[62:65]
	v_mfma_f32_16x16x128_f8f6f4 v[54:57], v[10:17], v[198:205], v[54:57]
	v_mfma_f32_16x16x128_f8f6f4 v[46:49], v[2:9], v[214:221], v[46:49]
	v_mfma_f32_16x16x128_f8f6f4 v[42:45], v[10:17], v[214:221], v[42:45]
	v_mfma_f32_16x16x128_f8f6f4 v[38:41], v[2:9], v[222:229], v[38:41]
	v_mfma_f32_16x16x128_f8f6f4 v[34:37], v[10:17], v[222:229], v[34:37]
	s_setprio 0
	s_barrier
	s_cmp_lg_u64 s[2:3], 0
	s_cbranch_scc0 .Ltx23_skip
	v_readfirstlane_b32 s23, v230
	s_mul_i32 s23, s23, 44
	s_add_i32 s23, s23, s79
	s_lshl_b32 s23, s23, 19
	s_mov_b32 s29, s23
.Ltx23_skip:
	ds_read_b128 v[2:5], v184
	ds_read_b128 v[6:9], v185
	ds_read_b128 v[10:13], v192
	ds_read_b128 v[14:17], v193
	ds_read_b128 v[18:21], v186
	ds_read_b128 v[22:25], v187
	ds_read_b128 v[26:29], v194
	ds_read_b128 v[30:33], v195
	v_mov_b32_e32 v172, v176
	ds_read_b128 v[164:167], v196 offset:32768
	ds_read_b128 v[168:171], v196 offset:33792
	ds_read_b128 v[198:201], v196 offset:34816
	ds_read_b128 v[202:205], v196 offset:35840
	ds_read_b128 v[214:217], v196 offset:36864
	ds_read_b128 v[218:221], v196 offset:37888
	ds_read_b128 v[222:225], v196 offset:38912
	ds_read_b128 v[226:229], v196 offset:39936
	s_add_i32 s86, s86, s47
	s_mov_b32 m0, s55
	v_add_u32_e32 v172, s86, v172
	global_load_lds_dwordx4 v172, s[4:5]
	v_mov_b32_e32 v172, v176
	s_add_i32 s86, s86, s47
	v_add_u32_e32 v172, s86, v172
	s_mov_b32 m0, s56
	s_nop 0
	global_load_lds_dwordx4 v172, s[4:5]
	s_waitcnt vmcnt(8)
	s_waitcnt lgkmcnt(0)
	s_barrier
	s_setprio 1
	s_waitcnt lgkmcnt(0)
	v_mfma_f32_16x16x128_f8f6f4 v[158:161], v[2:9], v[164:171], v[158:161]
	v_mfma_f32_16x16x128_f8f6f4 v[154:157], v[10:17], v[164:171], v[154:157]
	v_mfma_f32_16x16x128_f8f6f4 v[150:153], v[2:9], v[198:205], v[150:153]
	v_mfma_f32_16x16x128_f8f6f4 v[146:149], v[10:17], v[198:205], v[146:149]
	v_mfma_f32_16x16x128_f8f6f4 v[138:141], v[2:9], v[214:221], v[138:141]
	v_mfma_f32_16x16x128_f8f6f4 v[130:133], v[10:17], v[214:221], v[130:133]
	v_mfma_f32_16x16x128_f8f6f4 v[122:125], v[2:9], v[222:229], v[122:125]
	v_mfma_f32_16x16x128_f8f6f4 v[114:117], v[10:17], v[222:229], v[114:117]
	s_setprio 0
	s_setprio 1
	v_mfma_f32_16x16x128_f8f6f4 v[142:145], v[18:25], v[164:171], v[142:145]
	v_mfma_f32_16x16x128_f8f6f4 v[134:137], v[26:33], v[164:171], v[134:137]
	v_mfma_f32_16x16x128_f8f6f4 v[126:129], v[18:25], v[198:205], v[126:129]
	v_mfma_f32_16x16x128_f8f6f4 v[118:121], v[26:33], v[198:205], v[118:121]
	v_mfma_f32_16x16x128_f8f6f4 v[110:113], v[18:25], v[214:221], v[110:113]
	v_mfma_f32_16x16x128_f8f6f4 v[106:109], v[26:33], v[214:221], v[106:109]
	v_mfma_f32_16x16x128_f8f6f4 v[102:105], v[18:25], v[222:229], v[102:105]
	v_mfma_f32_16x16x128_f8f6f4 v[98:101], v[26:33], v[222:229], v[98:101]
	s_setprio 0
	s_barrier
	v_mov_b32_e32 v172, v177
	ds_read_b128 v[164:167], v196 offset:49152
	ds_read_b128 v[168:171], v196 offset:50176
	ds_read_b128 v[198:201], v196 offset:51200
	ds_read_b128 v[202:205], v196 offset:52224
	ds_read_b128 v[214:217], v196 offset:53248
	ds_read_b128 v[218:221], v196 offset:54272
	ds_read_b128 v[222:225], v196 offset:55296
	ds_read_b128 v[226:229], v196 offset:56320
	s_mov_b32 m0, s58
	v_add_u32_e32 v172, s85, v172
	global_load_lds_dwordx4 v172, s[6:7]
	v_mov_b32_e32 v172, v177
	s_add_i32 s85, s85, s48
	v_add_u32_e32 v172, s85, v172
	s_mov_b32 m0, s59
	s_add_i32 s85, s85, s48
	global_load_lds_dwordx4 v172, s[6:7]
	v_mov_b32_e32 v172, v177
	s_mov_b32 m0, s62
	v_add_u32_e32 v172, s85, v172
	global_load_lds_dwordx4 v172, s[6:7]
	v_mov_b32_e32 v172, v177
	s_add_i32 s85, s85, s48
	v_add_u32_e32 v172, s85, v172
	s_mov_b32 m0, s63
	s_nop 0
	global_load_lds_dwordx4 v172, s[6:7]
	v_mov_b32_e32 v172, v176
	s_mov_b32 m0, s60
	v_add_u32_e32 v172, s84, v172
	global_load_lds_dwordx4 v172, s[4:5]
	v_mov_b32_e32 v172, v176
	s_add_i32 s84, s84, s47
	v_add_u32_e32 v172, s84, v172
	s_mov_b32 m0, s61
	s_nop 0
	global_load_lds_dwordx4 v172, s[4:5]
	s_waitcnt vmcnt(8)
	s_waitcnt lgkmcnt(0)
	s_barrier
	s_setprio 1
	s_waitcnt lgkmcnt(0)
	v_mfma_f32_16x16x128_f8f6f4 v[94:97], v[2:9], v[164:171], v[94:97]
	v_mfma_f32_16x16x128_f8f6f4 v[90:93], v[10:17], v[164:171], v[90:93]
	v_mfma_f32_16x16x128_f8f6f4 v[86:89], v[2:9], v[198:205], v[86:89]
	v_mfma_f32_16x16x128_f8f6f4 v[82:85], v[10:17], v[198:205], v[82:85]
	v_mfma_f32_16x16x128_f8f6f4 v[74:77], v[2:9], v[214:221], v[74:77]
	v_mfma_f32_16x16x128_f8f6f4 v[66:69], v[10:17], v[214:221], v[66:69]
	v_mfma_f32_16x16x128_f8f6f4 v[58:61], v[2:9], v[222:229], v[58:61]
	v_mfma_f32_16x16x128_f8f6f4 v[50:53], v[10:17], v[222:229], v[50:53]
	s_setprio 0
	s_setprio 1
	v_mfma_f32_16x16x128_f8f6f4 v[78:81], v[18:25], v[164:171], v[78:81]
	v_mfma_f32_16x16x128_f8f6f4 v[70:73], v[26:33], v[164:171], v[70:73]
	v_mfma_f32_16x16x128_f8f6f4 v[62:65], v[18:25], v[198:205], v[62:65]
	v_mfma_f32_16x16x128_f8f6f4 v[54:57], v[26:33], v[198:205], v[54:57]
	v_mfma_f32_16x16x128_f8f6f4 v[46:49], v[18:25], v[214:221], v[46:49]
	v_mfma_f32_16x16x128_f8f6f4 v[42:45], v[26:33], v[214:221], v[42:45]
	v_mfma_f32_16x16x128_f8f6f4 v[38:41], v[18:25], v[222:229], v[38:41]
	v_mfma_f32_16x16x128_f8f6f4 v[34:37], v[26:33], v[222:229], v[34:37]
	s_setprio 0
	s_barrier
	s_add_i32 s83, s83, 2
	s_addk_i32 s28, 0x100
	s_addk_i32 s82, 0x100
	s_cmp_ge_i32 s83, s64
	s_cbranch_scc0 .LBB0_2937
	v_pk_fma_f32 v[164:165], v[160:161], s[18:19], 0 op_sel_hi:[1,0,0]
	v_pk_fma_f32 v[168:169], v[158:159], s[18:19], 0 op_sel_hi:[1,0,0]
	v_pk_fma_f32 v[172:173], v[144:145], s[20:21], 0 op_sel_hi:[1,0,0]
	v_pk_fma_f32 v[174:175], v[142:143], s[20:21], 0 op_sel_hi:[1,0,0]
	v_pk_fma_f32 v[156:157], v[156:157], s[18:19], 0 op_sel_hi:[1,0,0]
	v_pk_fma_f32 v[160:161], v[154:155], s[18:19], 0 op_sel_hi:[1,0,0]
	v_pk_fma_f32 v[166:167], v[136:137], s[20:21], 0 op_sel_hi:[1,0,0]
	v_pk_fma_f32 v[170:171], v[134:135], s[20:21], 0 op_sel_hi:[1,0,0]
	v_pk_fma_f32 v[152:153], v[152:153], s[18:19], 0 op_sel_hi:[1,0,0]
	v_pk_fma_f32 v[150:151], v[150:151], s[18:19], 0 op_sel_hi:[1,0,0]
	v_pk_fma_f32 v[154:155], v[128:129], s[20:21], 0 op_sel_hi:[1,0,0]
	v_pk_fma_f32 v[158:159], v[126:127], s[20:21], 0 op_sel_hi:[1,0,0]
	v_pk_fma_f32 v[142:143], v[148:149], s[18:19], 0 op_sel_hi:[1,0,0]
	v_pk_fma_f32 v[144:145], v[146:147], s[18:19], 0 op_sel_hi:[1,0,0]
	v_pk_fma_f32 v[146:147], v[120:121], s[20:21], 0 op_sel_hi:[1,0,0]
	v_pk_fma_f32 v[148:149], v[118:119], s[20:21], 0 op_sel_hi:[1,0,0]
	v_pk_fma_f32 v[134:135], v[140:141], s[18:19], 0 op_sel_hi:[1,0,0]
	v_pk_fma_f32 v[136:137], v[138:139], s[18:19], 0 op_sel_hi:[1,0,0]
	v_pk_fma_f32 v[138:139], v[112:113], s[20:21], 0 op_sel_hi:[1,0,0]
	v_pk_fma_f32 v[140:141], v[110:111], s[20:21], 0 op_sel_hi:[1,0,0]
	v_pk_fma_f32 v[126:127], v[132:133], s[18:19], 0 op_sel_hi:[1,0,0]
	v_pk_fma_f32 v[128:129], v[130:131], s[18:19], 0 op_sel_hi:[1,0,0]
	v_pk_fma_f32 v[130:131], v[108:109], s[20:21], 0 op_sel_hi:[1,0,0]
	v_pk_fma_f32 v[132:133], v[106:107], s[20:21], 0 op_sel_hi:[1,0,0]
	v_pk_fma_f32 v[108:109], v[124:125], s[18:19], 0 op_sel_hi:[1,0,0]
	v_pk_fma_f32 v[118:119], v[122:123], s[18:19], 0 op_sel_hi:[1,0,0]
	v_pk_fma_f32 v[120:121], v[104:105], s[20:21], 0 op_sel_hi:[1,0,0]
	v_pk_fma_f32 v[122:123], v[102:103], s[20:21], 0 op_sel_hi:[1,0,0]
	v_pk_fma_f32 v[102:103], v[116:117], s[18:19], 0 op_sel_hi:[1,0,0]
	v_pk_fma_f32 v[104:105], v[114:115], s[18:19], 0 op_sel_hi:[1,0,0]
	v_pk_fma_f32 v[106:107], v[100:101], s[20:21], 0 op_sel_hi:[1,0,0]
	v_pk_fma_f32 v[112:113], v[98:99], s[20:21], 0 op_sel_hi:[1,0,0]
	v_pk_fma_f32 v[96:97], v[96:97], s[18:19], 0 op_sel_hi:[1,0,0]
	v_pk_fma_f32 v[98:99], v[94:95], s[18:19], 0 op_sel_hi:[1,0,0]
	v_pk_fma_f32 v[100:101], v[80:81], s[20:21], 0 op_sel_hi:[1,0,0]
	v_pk_fma_f32 v[110:111], v[78:79], s[20:21], 0 op_sel_hi:[1,0,0]
	v_pk_fma_f32 v[78:79], v[92:93], s[18:19], 0 op_sel_hi:[1,0,0]
	v_pk_fma_f32 v[90:91], v[90:91], s[18:19], 0 op_sel_hi:[1,0,0]
	v_pk_fma_f32 v[92:93], v[72:73], s[20:21], 0 op_sel_hi:[1,0,0]
	v_pk_fma_f32 v[94:95], v[70:71], s[20:21], 0 op_sel_hi:[1,0,0]
	v_pk_fma_f32 v[70:71], v[88:89], s[18:19], 0 op_sel_hi:[1,0,0]
	v_pk_fma_f32 v[72:73], v[86:87], s[18:19], 0 op_sel_hi:[1,0,0]
	v_pk_fma_f32 v[64:65], v[64:65], s[20:21], 0 op_sel_hi:[1,0,0]
	v_pk_fma_f32 v[80:81], v[62:63], s[20:21], 0 op_sel_hi:[1,0,0]
	v_pk_fma_f32 v[32:33], v[84:85], s[18:19], 0 op_sel_hi:[1,0,0]
	v_pk_fma_f32 v[62:63], v[82:83], s[18:19], 0 op_sel_hi:[1,0,0]
	v_pk_fma_f32 v[56:57], v[56:57], s[20:21], 0 op_sel_hi:[1,0,0]
	v_pk_fma_f32 v[54:55], v[54:55], s[20:21], 0 op_sel_hi:[1,0,0]
	v_pk_fma_f32 v[24:25], v[76:77], s[18:19], 0 op_sel_hi:[1,0,0]
	v_pk_fma_f32 v[28:29], v[74:75], s[18:19], 0 op_sel_hi:[1,0,0]
	v_pk_fma_f32 v[30:31], v[48:49], s[20:21], 0 op_sel_hi:[1,0,0]
	v_pk_fma_f32 v[46:47], v[46:47], s[20:21], 0 op_sel_hi:[1,0,0]
	v_pk_fma_f32 v[16:17], v[68:69], s[18:19], 0 op_sel_hi:[1,0,0]
	v_pk_fma_f32 v[20:21], v[66:67], s[18:19], 0 op_sel_hi:[1,0,0]
	v_pk_fma_f32 v[22:23], v[44:45], s[20:21], 0 op_sel_hi:[1,0,0]
	v_pk_fma_f32 v[26:27], v[42:43], s[20:21], 0 op_sel_hi:[1,0,0]
	v_pk_fma_f32 v[8:9], v[60:61], s[18:19], 0 op_sel_hi:[1,0,0]
	v_pk_fma_f32 v[12:13], v[58:59], s[18:19], 0 op_sel_hi:[1,0,0]
	v_pk_fma_f32 v[14:15], v[40:41], s[20:21], 0 op_sel_hi:[1,0,0]
	v_pk_fma_f32 v[18:19], v[38:39], s[20:21], 0 op_sel_hi:[1,0,0]
	v_pk_fma_f32 v[2:3], v[52:53], s[18:19], 0 op_sel_hi:[1,0,0]
	v_pk_fma_f32 v[4:5], v[50:51], s[18:19], 0 op_sel_hi:[1,0,0]
	v_pk_fma_f32 v[6:7], v[36:37], s[20:21], 0 op_sel_hi:[1,0,0]
	v_pk_fma_f32 v[10:11], v[34:35], s[20:21], 0 op_sel_hi:[1,0,0]

.Lzs_11:
	v_mov_b64_e32 v[2:3], 0
	v_mov_b64_e32 v[4:5], 0
	v_mov_b64_e32 v[6:7], 0
	v_mov_b64_e32 v[8:9], 0
	v_mov_b64_e32 v[10:11], 0
	v_mov_b64_e32 v[12:13], 0
	v_mov_b64_e32 v[14:15], 0
	v_mov_b64_e32 v[16:17], 0
	v_mov_b64_e32 v[18:19], 0
	v_mov_b64_e32 v[20:21], 0
	v_mov_b64_e32 v[22:23], 0
	v_mov_b64_e32 v[24:25], 0
	v_mov_b64_e32 v[26:27], 0
	v_mov_b64_e32 v[28:29], 0
	v_mov_b64_e32 v[30:31], 0
	v_mov_b64_e32 v[32:33], 0
	v_mov_b64_e32 v[34:35], 0
	v_mov_b64_e32 v[36:37], 0
	v_mov_b64_e32 v[38:39], 0
	v_mov_b64_e32 v[40:41], 0
	v_mov_b64_e32 v[42:43], 0
	v_mov_b64_e32 v[44:45], 0
	v_mov_b64_e32 v[46:47], 0
	v_mov_b64_e32 v[48:49], 0
	v_mov_b64_e32 v[54:55], 0
	v_mov_b64_e32 v[56:57], 0
	v_mov_b64_e32 v[62:63], 0
	v_mov_b64_e32 v[64:65], 0
	v_mov_b64_e32 v[66:67], 0
	v_mov_b64_e32 v[68:69], 0
	v_mov_b64_e32 v[70:71], 0
	v_mov_b64_e32 v[72:73], 0
	v_mov_b64_e32 v[74:75], 0
	v_mov_b64_e32 v[76:77], 0
	v_mov_b64_e32 v[78:79], 0
	v_mov_b64_e32 v[80:81], 0
	v_mov_b64_e32 v[82:83], 0
	v_mov_b64_e32 v[84:85], 0
	v_mov_b64_e32 v[86:87], 0
	v_mov_b64_e32 v[88:89], 0
	v_mov_b64_e32 v[90:91], 0
	v_mov_b64_e32 v[92:93], 0
	v_mov_b64_e32 v[94:95], 0
	v_mov_b64_e32 v[96:97], 0
	v_mov_b64_e32 v[98:99], 0
	v_mov_b64_e32 v[100:101], 0
	v_mov_b64_e32 v[102:103], 0
	v_mov_b64_e32 v[104:105], 0
	v_mov_b64_e32 v[106:107], 0
	v_mov_b64_e32 v[108:109], 0
	v_mov_b64_e32 v[110:111], 0
	v_mov_b64_e32 v[112:113], 0
	v_mov_b64_e32 v[114:115], 0
	v_mov_b64_e32 v[116:117], 0
	v_mov_b64_e32 v[118:119], 0
	v_mov_b64_e32 v[120:121], 0
	v_mov_b64_e32 v[122:123], 0
	v_mov_b64_e32 v[124:125], 0
	v_mov_b64_e32 v[126:127], 0
	v_mov_b64_e32 v[128:129], 0
	v_mov_b64_e32 v[134:135], 0
	v_mov_b64_e32 v[136:137], 0
	v_mov_b64_e32 v[142:143], 0
	v_mov_b64_e32 v[144:145], 0
	s_branch .LBB0_3009

.LBB0_3003:
	s_add_i32 s49, s49, 1
	s_mul_i32 s2, s49, s63
	s_mul_hi_u32 s3, s49, s34
	s_add_i32 s3, s3, s2
	s_mul_i32 s2, s49, s34
	s_add_u32 s20, s2, s26
	s_addc_u32 s21, s3, s28
	v_cmp_ge_i64_e32 vcc, s[20:21], v[162:163]
	v_cmp_lt_i64_e64 s[2:3], s[20:21], v[162:163]
	s_mov_b32 s21, s75
	s_mov_b32 s11, s74
	s_cbranch_vccnz .LBB0_3005
	s_ashr_i32 s11, s20, 31
	s_lshr_b32 s11, s11, 29
	s_add_i32 s11, s20, s11
	s_ashr_i32 s18, s11, 3
	s_and_b32 s11, s11, -8
	s_sub_i32 s11, s20, s11
	s_cmp_lt_i32 s11, 0
	s_cselect_b32 s19, s29, s17
	s_mul_i32 s11, s11, s19
	s_add_i32 s11, s11, s18
	s_ashr_i32 s18, s11, 31
	s_lshr_b32 s18, s18, 26
	s_add_i32 s18, s11, s18
	s_ashr_i32 s19, s18, 6
	s_lshl_b32 s19, s19, 3
	s_sub_i32 s20, s17, s19
	s_min_i32 s20, s20, 8
	s_abs_i32 s21, s20
	v_cvt_f32_u32_e32 v2, s21
	s_sub_i32 s73, 0, s21
	s_andn2_b32 s18, s18, 63
	s_sub_i32 s11, s11, s18
	v_rcp_iflag_f32_e32 v2, v2
	s_abs_i32 s18, s11
	s_xor_b32 s72, s11, s20
	s_ashr_i32 s72, s72, 31
	v_mul_f32_e32 v2, 0x4f7ffffe, v2
	v_cvt_u32_f32_e32 v2, v2
	s_nop 0
	v_readfirstlane_b32 s76, v2
	s_mul_i32 s73, s73, s76
	s_mul_hi_u32 s73, s76, s73
	s_add_i32 s76, s76, s73
	s_mul_hi_u32 s73, s18, s76
	s_mul_i32 s76, s73, s21
	s_sub_i32 s18, s18, s76
	s_add_i32 s77, s73, 1
	s_sub_i32 s76, s18, s21
	s_cmp_ge_u32 s18, s21
	s_cselect_b32 s73, s77, s73
	s_cselect_b32 s18, s76, s18
	s_add_i32 s76, s73, 1
	s_cmp_ge_u32 s18, s21
	s_cselect_b32 s18, s76, s73
	s_xor_b32 s18, s18, s72
	s_sub_i32 s72, s18, s72
	s_mul_i32 s18, s72, s20
	s_sub_i32 s11, s11, s18
	s_add_i32 s18, s19, s11
	s_ashr_i32 s19, s18, 31
	s_lshl_b64 s[20:21], s[18:19], 2
	s_add_u32 s20, s22, s20
	s_addc_u32 s21, s23, s21
	global_load_dword v230, v1, s[20:21]
	s_mul_i32 s11, s18, 0x160000
	s_mov_b32 s73, s11
.LBB0_3005:
	s_andn2_b64 vcc, exec, s[12:13]
	v_mov_b64_e32 v[2:3], 0
	v_mov_b64_e32 v[4:5], 0
	v_mov_b64_e32 v[6:7], 0
	v_mov_b64_e32 v[8:9], 0
	v_mov_b64_e32 v[10:11], 0
	v_mov_b64_e32 v[12:13], 0
	v_mov_b64_e32 v[14:15], 0
	v_mov_b64_e32 v[16:17], 0
	v_mov_b64_e32 v[18:19], 0
	v_mov_b64_e32 v[20:21], 0
	v_mov_b64_e32 v[22:23], 0
	v_mov_b64_e32 v[24:25], 0
	v_mov_b64_e32 v[26:27], 0
	v_mov_b64_e32 v[28:29], 0
	v_mov_b64_e32 v[30:31], 0
	v_mov_b64_e32 v[32:33], 0
	s_cbranch_vccnz .Lzs_11
	s_add_i32 s20, s74, 0x80
	s_add_i32 s74, s75, 0x100
	s_mov_b32 s75, 0
	v_mov_b64_e32 v[34:35], 0
	v_mov_b64_e32 v[36:37], 0
	v_mov_b64_e32 v[38:39], 0
	v_mov_b64_e32 v[40:41], 0
	v_mov_b64_e32 v[42:43], 0
	v_mov_b64_e32 v[44:45], 0
	v_mov_b64_e32 v[46:47], 0
	v_mov_b64_e32 v[48:49], 0
	v_mov_b64_e32 v[50:51], 0
	v_mov_b64_e32 v[52:53], 0
	v_mov_b64_e32 v[54:55], 0
	v_mov_b64_e32 v[56:57], 0
	v_mov_b64_e32 v[58:59], 0
	v_mov_b64_e32 v[60:61], 0
	v_mov_b64_e32 v[62:63], 0
	v_mov_b64_e32 v[64:65], 0
	v_mov_b64_e32 v[66:67], 0
	v_mov_b64_e32 v[68:69], 0
	v_mov_b64_e32 v[70:71], 0
	v_mov_b64_e32 v[72:73], 0
	v_mov_b64_e32 v[74:75], 0
	v_mov_b64_e32 v[76:77], 0
	v_mov_b64_e32 v[78:79], 0
	v_mov_b64_e32 v[80:81], 0
	v_mov_b64_e32 v[82:83], 0
	v_mov_b64_e32 v[84:85], 0
	v_mov_b64_e32 v[86:87], 0
	v_mov_b64_e32 v[88:89], 0
	v_mov_b64_e32 v[90:91], 0
	v_mov_b64_e32 v[92:93], 0
	v_mov_b64_e32 v[94:95], 0
	v_mov_b64_e32 v[96:97], 0
	v_mov_b64_e32 v[98:99], 0
	v_mov_b64_e32 v[100:101], 0
	v_mov_b64_e32 v[102:103], 0
	v_mov_b64_e32 v[104:105], 0
	v_mov_b64_e32 v[106:107], 0
	v_mov_b64_e32 v[108:109], 0
	v_mov_b64_e32 v[110:111], 0
	v_mov_b64_e32 v[112:113], 0
	v_mov_b64_e32 v[114:115], 0
	v_mov_b64_e32 v[116:117], 0
	v_mov_b64_e32 v[118:119], 0
	v_mov_b64_e32 v[120:121], 0
	v_mov_b64_e32 v[122:123], 0
	v_mov_b64_e32 v[124:125], 0
	v_mov_b64_e32 v[126:127], 0
	v_mov_b64_e32 v[128:129], 0
	v_mov_b64_e32 v[130:131], 0
	v_mov_b64_e32 v[132:133], 0
	v_mov_b64_e32 v[134:135], 0
	v_mov_b64_e32 v[136:137], 0
	v_mov_b64_e32 v[138:139], 0
	v_mov_b64_e32 v[140:141], 0
	v_mov_b64_e32 v[142:143], 0
	v_mov_b64_e32 v[144:145], 0
	v_mov_b64_e32 v[146:147], 0
	v_mov_b64_e32 v[148:149], 0
	v_mov_b64_e32 v[150:151], 0
	v_mov_b64_e32 v[152:153], 0
	v_mov_b64_e32 v[154:155], 0
	v_mov_b64_e32 v[156:157], 0
	v_mov_b64_e32 v[158:159], 0
	v_mov_b64_e32 v[160:161], 0
.LBB0_3007:
	ds_read_b128 v[18:21], v168
	ds_read_b128 v[22:25], v169
	ds_read_b128 v[26:29], v176
	ds_read_b128 v[30:33], v177
	ds_read_b128 v[2:5], v170
	ds_read_b128 v[6:9], v171
	ds_read_b128 v[10:13], v178
	ds_read_b128 v[14:17], v179
	s_add_i32 s76, s20, 0x80
	s_cmp_eq_u32 s61, s75
	s_cselect_b32 s78, s11, s76
	s_cselect_b32 s77, s21, s74
	s_add_i32 s76, s78, 0x80
	v_mov_b32_e32 v185, v164
	ds_read_b128 v[186:189], v184
	ds_read_b128 v[190:193], v184 offset:1024
	ds_read_b128 v[194:197], v184 offset:2048
	ds_read_b128 v[198:201], v184 offset:3072
	ds_read_b128 v[202:205], v184 offset:4096
	ds_read_b128 v[206:209], v184 offset:5120
	ds_read_b128 v[214:217], v184 offset:6144
	ds_read_b128 v[218:221], v184 offset:7168
	s_add_i32 s79, s20, s59
	v_add_u32_e32 v185, s79, v185
	s_add_i32 m0, s30, 0xc000
	s_add_i32 s79, s20, s66
	global_load_lds_dwordx4 v185, s[4:5]
	v_mov_b32_e32 v185, v164
	s_add_i32 m0, s30, 0xe000
	v_add_u32_e32 v185, s79, v185
	global_load_lds_dwordx4 v185, s[4:5]
	s_waitcnt vmcnt(8)
	s_waitcnt lgkmcnt(0)
	s_barrier
	s_setprio 1
	s_waitcnt lgkmcnt(0)
	v_mfma_f32_16x16x128_f8f6f4 v[158:161], v[18:25], v[186:193], v[158:161]
	v_mfma_f32_16x16x128_f8f6f4 v[154:157], v[26:33], v[186:193], v[154:157]
	v_mfma_f32_16x16x128_f8f6f4 v[150:153], v[18:25], v[194:201], v[150:153]
	v_mfma_f32_16x16x128_f8f6f4 v[146:149], v[26:33], v[194:201], v[146:149]
	v_mfma_f32_16x16x128_f8f6f4 v[138:141], v[18:25], v[202:209], v[138:141]
	v_mfma_f32_16x16x128_f8f6f4 v[130:133], v[26:33], v[202:209], v[130:133]
	v_mfma_f32_16x16x128_f8f6f4 v[122:125], v[18:25], v[214:221], v[122:125]
	v_mfma_f32_16x16x128_f8f6f4 v[114:117], v[26:33], v[214:221], v[114:117]
	s_setprio 0
	s_setprio 1
	v_mfma_f32_16x16x128_f8f6f4 v[142:145], v[2:9], v[186:193], v[142:145]
	v_mfma_f32_16x16x128_f8f6f4 v[134:137], v[10:17], v[186:193], v[134:137]
	v_mfma_f32_16x16x128_f8f6f4 v[126:129], v[2:9], v[194:201], v[126:129]
	v_mfma_f32_16x16x128_f8f6f4 v[118:121], v[10:17], v[194:201], v[118:121]
	v_mfma_f32_16x16x128_f8f6f4 v[110:113], v[2:9], v[202:209], v[110:113]
	v_mfma_f32_16x16x128_f8f6f4 v[106:109], v[10:17], v[202:209], v[106:109]
	v_mfma_f32_16x16x128_f8f6f4 v[102:105], v[2:9], v[214:221], v[102:105]
	v_mfma_f32_16x16x128_f8f6f4 v[98:101], v[10:17], v[214:221], v[98:101]
	s_setprio 0
	s_barrier
	v_mov_b32_e32 v185, v165
	ds_read_b128 v[186:189], v184 offset:16384
	ds_read_b128 v[190:193], v184 offset:17408
	ds_read_b128 v[194:197], v184 offset:18432
	ds_read_b128 v[198:201], v184 offset:19456
	ds_read_b128 v[202:205], v184 offset:20480
	ds_read_b128 v[206:209], v184 offset:21504
	ds_read_b128 v[214:217], v184 offset:22528
	ds_read_b128 v[218:221], v184 offset:23552
	s_mov_b32 m0, s31
	v_add_u32_e32 v185, s77, v185
	global_load_lds_dwordx4 v185, s[6:7]
	v_mov_b32_e32 v185, v165
	s_add_i32 s79, s77, s25
	v_add_u32_e32 v185, s79, v185
	s_mov_b32 m0, s35
	s_add_i32 s79, s79, s25
	global_load_lds_dwordx4 v185, s[6:7]
	v_mov_b32_e32 v185, v165
	s_mov_b32 m0, s44
	v_add_u32_e32 v185, s79, v185
	global_load_lds_dwordx4 v185, s[6:7]
	v_mov_b32_e32 v185, v165
	s_add_i32 s79, s79, s25
	v_add_u32_e32 v185, s79, v185
	s_mov_b32 m0, s45
	s_nop 0
	global_load_lds_dwordx4 v185, s[6:7]
	v_mov_b32_e32 v185, v164
	s_mov_b32 m0, s30
	v_add_u32_e32 v185, s78, v185
	global_load_lds_dwordx4 v185, s[4:5]
	v_mov_b32_e32 v185, v164
	s_add_i32 s78, s78, s24
	v_add_u32_e32 v185, s78, v185
	s_mov_b32 m0, s46
	s_nop 0
	global_load_lds_dwordx4 v185, s[4:5]
	s_waitcnt vmcnt(8)
	s_waitcnt lgkmcnt(0)
	s_barrier
	s_setprio 1
	s_waitcnt lgkmcnt(0)
	v_mfma_f32_16x16x128_f8f6f4 v[94:97], v[18:25], v[186:193], v[94:97]
	v_mfma_f32_16x16x128_f8f6f4 v[90:93], v[26:33], v[186:193], v[90:93]
	v_mfma_f32_16x16x128_f8f6f4 v[86:89], v[18:25], v[194:201], v[86:89]
	v_mfma_f32_16x16x128_f8f6f4 v[82:85], v[26:33], v[194:201], v[82:85]
	v_mfma_f32_16x16x128_f8f6f4 v[74:77], v[18:25], v[202:209], v[74:77]
	v_mfma_f32_16x16x128_f8f6f4 v[66:69], v[26:33], v[202:209], v[66:69]
	v_mfma_f32_16x16x128_f8f6f4 v[58:61], v[18:25], v[214:221], v[58:61]
	v_mfma_f32_16x16x128_f8f6f4 v[50:53], v[26:33], v[214:221], v[50:53]
	s_setprio 0
	s_setprio 1
	v_mfma_f32_16x16x128_f8f6f4 v[78:81], v[2:9], v[186:193], v[78:81]
	v_mfma_f32_16x16x128_f8f6f4 v[70:73], v[10:17], v[186:193], v[70:73]
	v_mfma_f32_16x16x128_f8f6f4 v[62:65], v[2:9], v[194:201], v[62:65]
	v_mfma_f32_16x16x128_f8f6f4 v[54:57], v[10:17], v[194:201], v[54:57]
	v_mfma_f32_16x16x128_f8f6f4 v[46:49], v[2:9], v[202:209], v[46:49]
	v_mfma_f32_16x16x128_f8f6f4 v[42:45], v[10:17], v[202:209], v[42:45]
	v_mfma_f32_16x16x128_f8f6f4 v[38:41], v[2:9], v[214:221], v[38:41]
	v_mfma_f32_16x16x128_f8f6f4 v[34:37], v[10:17], v[214:221], v[34:37]
	s_setprio 0
	s_barrier
	s_cmp_lg_u64 s[2:3], 0
	s_cbranch_scc0 .Ltx24_skip
	v_readfirstlane_b32 s19, v230
	s_lshl_b32 s19, s19, 3
	s_add_i32 s19, s19, s72
	s_mul_i32 s21, s19, 0x160000
	s_mov_b32 s19, s21
.Ltx24_skip:
	ds_read_b128 v[2:5], v172
	ds_read_b128 v[6:9], v173
	ds_read_b128 v[10:13], v180
	ds_read_b128 v[14:17], v181
	ds_read_b128 v[18:21], v174
	ds_read_b128 v[22:25], v175
	ds_read_b128 v[26:29], v182
	ds_read_b128 v[30:33], v183
	v_mov_b32_e32 v185, v164
	ds_read_b128 v[186:189], v184 offset:32768
	ds_read_b128 v[190:193], v184 offset:33792
	ds_read_b128 v[194:197], v184 offset:34816
	ds_read_b128 v[198:201], v184 offset:35840
	ds_read_b128 v[202:205], v184 offset:36864
	ds_read_b128 v[206:209], v184 offset:37888
	ds_read_b128 v[214:217], v184 offset:38912
	ds_read_b128 v[218:221], v184 offset:39936
	s_add_i32 s78, s78, s24
	s_mov_b32 m0, s47
	v_add_u32_e32 v185, s78, v185
	global_load_lds_dwordx4 v185, s[4:5]
	v_mov_b32_e32 v185, v164
	s_add_i32 s78, s78, s24
	v_add_u32_e32 v185, s78, v185
	s_mov_b32 m0, s48
	s_nop 0
	global_load_lds_dwordx4 v185, s[4:5]
	s_waitcnt vmcnt(8)
	s_waitcnt lgkmcnt(0)
	s_barrier
	s_setprio 1
	s_waitcnt lgkmcnt(0)
	v_mfma_f32_16x16x128_f8f6f4 v[158:161], v[2:9], v[186:193], v[158:161]
	v_mfma_f32_16x16x128_f8f6f4 v[154:157], v[10:17], v[186:193], v[154:157]
	v_mfma_f32_16x16x128_f8f6f4 v[150:153], v[2:9], v[194:201], v[150:153]
	v_mfma_f32_16x16x128_f8f6f4 v[146:149], v[10:17], v[194:201], v[146:149]
	v_mfma_f32_16x16x128_f8f6f4 v[138:141], v[2:9], v[202:209], v[138:141]
	v_mfma_f32_16x16x128_f8f6f4 v[130:133], v[10:17], v[202:209], v[130:133]
	v_mfma_f32_16x16x128_f8f6f4 v[122:125], v[2:9], v[214:221], v[122:125]
	v_mfma_f32_16x16x128_f8f6f4 v[114:117], v[10:17], v[214:221], v[114:117]
	s_setprio 0
	s_setprio 1
	v_mfma_f32_16x16x128_f8f6f4 v[142:145], v[18:25], v[186:193], v[142:145]
	v_mfma_f32_16x16x128_f8f6f4 v[134:137], v[26:33], v[186:193], v[134:137]
	v_mfma_f32_16x16x128_f8f6f4 v[126:129], v[18:25], v[194:201], v[126:129]
	v_mfma_f32_16x16x128_f8f6f4 v[118:121], v[26:33], v[194:201], v[118:121]
	v_mfma_f32_16x16x128_f8f6f4 v[110:113], v[18:25], v[202:209], v[110:113]
	v_mfma_f32_16x16x128_f8f6f4 v[106:109], v[26:33], v[202:209], v[106:109]
	v_mfma_f32_16x16x128_f8f6f4 v[102:105], v[18:25], v[214:221], v[102:105]
	v_mfma_f32_16x16x128_f8f6f4 v[98:101], v[26:33], v[214:221], v[98:101]
	s_setprio 0
	s_barrier
	v_mov_b32_e32 v185, v165
	ds_read_b128 v[186:189], v184 offset:49152
	ds_read_b128 v[190:193], v184 offset:50176
	ds_read_b128 v[194:197], v184 offset:51200
	ds_read_b128 v[198:201], v184 offset:52224
	ds_read_b128 v[202:205], v184 offset:53248
	ds_read_b128 v[206:209], v184 offset:54272
	ds_read_b128 v[214:217], v184 offset:55296
	ds_read_b128 v[218:221], v184 offset:56320
	s_addk_i32 s77, 0x80
	s_mov_b32 m0, s51
	v_add_u32_e32 v185, s77, v185
	global_load_lds_dwordx4 v185, s[6:7]
	v_mov_b32_e32 v185, v165
	s_add_i32 s77, s77, s25
	v_add_u32_e32 v185, s77, v185
	s_mov_b32 m0, s52
	s_add_i32 s77, s77, s25
	global_load_lds_dwordx4 v185, s[6:7]
	v_mov_b32_e32 v185, v165
	s_mov_b32 m0, s55
	v_add_u32_e32 v185, s77, v185
	global_load_lds_dwordx4 v185, s[6:7]
	v_mov_b32_e32 v185, v165
	s_add_i32 s77, s77, s25
	v_add_u32_e32 v185, s77, v185
	s_mov_b32 m0, s57
	s_nop 0
	global_load_lds_dwordx4 v185, s[6:7]
	v_mov_b32_e32 v185, v164
	s_mov_b32 m0, s53
	v_add_u32_e32 v185, s76, v185
	global_load_lds_dwordx4 v185, s[4:5]
	v_mov_b32_e32 v185, v164
	s_add_i32 s76, s76, s24
	v_add_u32_e32 v185, s76, v185
	s_mov_b32 m0, s54
	s_nop 0
	global_load_lds_dwordx4 v185, s[4:5]
	s_waitcnt vmcnt(8)
	s_waitcnt lgkmcnt(0)
	s_barrier
	s_setprio 1
	s_waitcnt lgkmcnt(0)
	v_mfma_f32_16x16x128_f8f6f4 v[94:97], v[2:9], v[186:193], v[94:97]
	v_mfma_f32_16x16x128_f8f6f4 v[90:93], v[10:17], v[186:193], v[90:93]
	v_mfma_f32_16x16x128_f8f6f4 v[86:89], v[2:9], v[194:201], v[86:89]
	v_mfma_f32_16x16x128_f8f6f4 v[82:85], v[10:17], v[194:201], v[82:85]
	v_mfma_f32_16x16x128_f8f6f4 v[74:77], v[2:9], v[202:209], v[74:77]
	v_mfma_f32_16x16x128_f8f6f4 v[66:69], v[10:17], v[202:209], v[66:69]
	v_mfma_f32_16x16x128_f8f6f4 v[58:61], v[2:9], v[214:221], v[58:61]
	v_mfma_f32_16x16x128_f8f6f4 v[50:53], v[10:17], v[214:221], v[50:53]
	s_setprio 0
	s_setprio 1
	v_mfma_f32_16x16x128_f8f6f4 v[78:81], v[18:25], v[186:193], v[78:81]
	v_mfma_f32_16x16x128_f8f6f4 v[70:73], v[26:33], v[186:193], v[70:73]
	v_mfma_f32_16x16x128_f8f6f4 v[62:65], v[18:25], v[194:201], v[62:65]
	v_mfma_f32_16x16x128_f8f6f4 v[54:57], v[26:33], v[194:201], v[54:57]
	v_mfma_f32_16x16x128_f8f6f4 v[46:49], v[18:25], v[202:209], v[46:49]
	v_mfma_f32_16x16x128_f8f6f4 v[42:45], v[26:33], v[202:209], v[42:45]
	v_mfma_f32_16x16x128_f8f6f4 v[38:41], v[18:25], v[214:221], v[38:41]
	v_mfma_f32_16x16x128_f8f6f4 v[34:37], v[26:33], v[214:221], v[34:37]
	s_setprio 0
	s_barrier
	s_add_i32 s75, s75, 2
	s_addk_i32 s20, 0x100
	s_addk_i32 s74, 0x100
	s_cmp_ge_i32 s75, s58
	s_cbranch_scc0 .LBB0_3007
	v_pk_mul_f32 v[2:3], v[160:161], s[16:17] op_sel_hi:[1,0]
	v_pk_mul_f32 v[4:5], v[158:159], s[16:17] op_sel_hi:[1,0]
	v_pk_mul_f32 v[6:7], v[156:157], s[16:17] op_sel_hi:[1,0]
	v_pk_mul_f32 v[12:13], v[154:155], s[16:17] op_sel_hi:[1,0]
	v_pk_mul_f32 v[144:145], v[144:145], s[16:17] op_sel_hi:[1,0]
	v_pk_mul_f32 v[142:143], v[142:143], s[16:17] op_sel_hi:[1,0]
	v_pk_mul_f32 v[136:137], v[136:137], s[16:17] op_sel_hi:[1,0]
	v_pk_mul_f32 v[134:135], v[134:135], s[16:17] op_sel_hi:[1,0]
	v_pk_mul_f32 v[8:9], v[152:153], s[16:17] op_sel_hi:[1,0]
	v_pk_mul_f32 v[14:15], v[150:151], s[16:17] op_sel_hi:[1,0]
	v_pk_mul_f32 v[18:19], v[148:149], s[16:17] op_sel_hi:[1,0]
	v_pk_mul_f32 v[26:27], v[146:147], s[16:17] op_sel_hi:[1,0]
	v_pk_mul_f32 v[128:129], v[128:129], s[16:17] op_sel_hi:[1,0]
	v_pk_mul_f32 v[126:127], v[126:127], s[16:17] op_sel_hi:[1,0]
	v_pk_mul_f32 v[120:121], v[120:121], s[16:17] op_sel_hi:[1,0]
	v_pk_mul_f32 v[118:119], v[118:119], s[16:17] op_sel_hi:[1,0]
	v_pk_mul_f32 v[10:11], v[140:141], s[16:17] op_sel_hi:[1,0]
	v_pk_mul_f32 v[20:21], v[138:139], s[16:17] op_sel_hi:[1,0]
	v_pk_mul_f32 v[22:23], v[132:133], s[16:17] op_sel_hi:[1,0]
	v_pk_mul_f32 v[30:31], v[130:131], s[16:17] op_sel_hi:[1,0]
	v_pk_mul_f32 v[112:113], v[112:113], s[16:17] op_sel_hi:[1,0]
	v_pk_mul_f32 v[110:111], v[110:111], s[16:17] op_sel_hi:[1,0]
	v_pk_mul_f32 v[108:109], v[108:109], s[16:17] op_sel_hi:[1,0]
	v_pk_mul_f32 v[106:107], v[106:107], s[16:17] op_sel_hi:[1,0]
	v_pk_mul_f32 v[16:17], v[124:125], s[16:17] op_sel_hi:[1,0]
	v_pk_mul_f32 v[24:25], v[122:123], s[16:17] op_sel_hi:[1,0]
	v_pk_mul_f32 v[28:29], v[116:117], s[16:17] op_sel_hi:[1,0]
	v_pk_mul_f32 v[32:33], v[114:115], s[16:17] op_sel_hi:[1,0]
	v_pk_mul_f32 v[104:105], v[104:105], s[16:17] op_sel_hi:[1,0]
	v_pk_mul_f32 v[102:103], v[102:103], s[16:17] op_sel_hi:[1,0]
	v_pk_mul_f32 v[100:101], v[100:101], s[16:17] op_sel_hi:[1,0]
	v_pk_mul_f32 v[98:99], v[98:99], s[16:17] op_sel_hi:[1,0]
	v_pk_mul_f32 v[96:97], v[96:97], s[16:17] op_sel_hi:[1,0]
	v_pk_mul_f32 v[94:95], v[94:95], s[16:17] op_sel_hi:[1,0]
	v_pk_mul_f32 v[92:93], v[92:93], s[16:17] op_sel_hi:[1,0]
	v_pk_mul_f32 v[90:91], v[90:91], s[16:17] op_sel_hi:[1,0]
	v_pk_mul_f32 v[114:115], v[80:81], s[16:17] op_sel_hi:[1,0]
	v_pk_mul_f32 v[116:117], v[78:79], s[16:17] op_sel_hi:[1,0]
	v_pk_mul_f32 v[122:123], v[72:73], s[16:17] op_sel_hi:[1,0]
	v_pk_mul_f32 v[124:125], v[70:71], s[16:17] op_sel_hi:[1,0]
	v_pk_mul_f32 v[70:71], v[88:89], s[16:17] op_sel_hi:[1,0]
	v_pk_mul_f32 v[72:73], v[86:87], s[16:17] op_sel_hi:[1,0]
	v_pk_mul_f32 v[78:79], v[84:85], s[16:17] op_sel_hi:[1,0]
	v_pk_mul_f32 v[80:81], v[82:83], s[16:17] op_sel_hi:[1,0]
	v_pk_mul_f32 v[82:83], v[64:65], s[16:17] op_sel_hi:[1,0]
	v_pk_mul_f32 v[84:85], v[62:63], s[16:17] op_sel_hi:[1,0]
	v_pk_mul_f32 v[86:87], v[56:57], s[16:17] op_sel_hi:[1,0]
	v_pk_mul_f32 v[88:89], v[54:55], s[16:17] op_sel_hi:[1,0]
	v_pk_mul_f32 v[54:55], v[76:77], s[16:17] op_sel_hi:[1,0]
	v_pk_mul_f32 v[56:57], v[74:75], s[16:17] op_sel_hi:[1,0]
	v_pk_mul_f32 v[62:63], v[68:69], s[16:17] op_sel_hi:[1,0]
	v_pk_mul_f32 v[64:65], v[66:67], s[16:17] op_sel_hi:[1,0]
	v_pk_mul_f32 v[66:67], v[48:49], s[16:17] op_sel_hi:[1,0]
	v_pk_mul_f32 v[68:69], v[46:47], s[16:17] op_sel_hi:[1,0]
	v_pk_mul_f32 v[74:75], v[44:45], s[16:17] op_sel_hi:[1,0]
	v_pk_mul_f32 v[76:77], v[42:43], s[16:17] op_sel_hi:[1,0]
	v_pk_mul_f32 v[42:43], v[60:61], s[16:17] op_sel_hi:[1,0]
	v_pk_mul_f32 v[44:45], v[58:59], s[16:17] op_sel_hi:[1,0]
	v_pk_mul_f32 v[46:47], v[52:53], s[16:17] op_sel_hi:[1,0]
	v_pk_mul_f32 v[48:49], v[50:51], s[16:17] op_sel_hi:[1,0]
	v_pk_mul_f32 v[40:41], v[40:41], s[16:17] op_sel_hi:[1,0]
	v_pk_mul_f32 v[38:39], v[38:39], s[16:17] op_sel_hi:[1,0]
	v_pk_mul_f32 v[36:37], v[36:37], s[16:17] op_sel_hi:[1,0]
	v_pk_mul_f32 v[34:35], v[34:35], s[16:17] op_sel_hi:[1,0]
